# expert weight conversion: default cache policy instead of nt on its loads and stores
# speedup vs baseline: 1.0085x; 1.0085x over previous
.LBB0_168:
	s_andn2_b64 vcc, exec, s[4:5]
	s_cbranch_vccnz .LBB0_182
	v_lshrrev_b32_e32 v1, 1, v67
	s_and_b32 s30, s1, 15
	v_and_b32_e32 v1, 24, v1
	v_lshl_or_b32 v8, s30, 7, v1
	v_lshlrev_b32_e32 v2, 2, v67
	v_and_b32_e32 v66, 60, v2
	v_mul_u32_u24_e32 v2, s27, v8
	s_mov_b32 s9, 0
	s_lshl_b32 s8, s29, 8
	v_mov_b32_e32 v131, 0
	v_lshlrev_b32_e32 v130, 2, v2
	v_lshl_add_u64 v[2:3], s[18:19], 0, v[130:131]
	s_lshl_b64 s[6:7], s[8:9], 2
	s_lshl_b32 s8, s27, 2
	v_lshl_add_u64 v[4:5], v[2:3], 0, s[6:7]
	v_lshlrev_b32_e32 v130, 2, v66
	v_lshl_add_u64 v[2:3], v[2:3], 0, s[8:9]
	s_add_i32 s1, s27, s27
	v_lshl_add_u64 v[4:5], v[4:5], 0, v[130:131]
	v_lshl_add_u64 v[6:7], v[2:3], 0, s[6:7]
	s_add_i32 s1, s1, s27
	v_lshl_add_u64 v[6:7], v[6:7], 0, v[130:131]
	global_load_dwordx4 v[58:61], v[4:5], off
	global_load_dwordx4 v[62:65], v[6:7], off
	v_mov_b32_e32 v4, s1
	v_mad_u32_u24 v6, v8, s27, v4
	v_lshlrev_b32_e32 v4, 2, v6
	v_mov_b32_e32 v5, v131
	v_lshl_add_u64 v[2:3], v[2:3], 0, s[8:9]
	v_lshl_add_u64 v[4:5], s[18:19], 0, v[4:5]
	v_lshl_add_u64 v[2:3], v[2:3], 0, s[6:7]
	v_lshl_add_u64 v[4:5], v[4:5], 0, s[6:7]
	v_lshl_add_u64 v[2:3], v[2:3], 0, v[130:131]
	v_lshl_add_u64 v[4:5], v[4:5], 0, v[130:131]
	global_load_dwordx4 v[50:53], v[2:3], off
	global_load_dwordx4 v[42:45], v[4:5], off
	v_add_u32_e32 v4, s27, v6
	v_lshlrev_b32_e32 v2, 2, v4
	v_mov_b32_e32 v3, v131
	v_lshl_add_u64 v[2:3], s[18:19], 0, v[2:3]
	v_add_u32_e32 v4, s27, v4
	v_mov_b32_e32 v5, v131
	v_lshl_add_u64 v[2:3], v[2:3], 0, s[6:7]
	v_lshl_add_u64 v[6:7], v[4:5], 2, s[18:19]
	v_lshl_add_u64 v[2:3], v[2:3], 0, v[130:131]
	v_lshl_add_u64 v[6:7], v[6:7], 0, s[6:7]
	v_lshl_add_u64 v[6:7], v[6:7], 0, v[130:131]
	global_load_dwordx4 v[54:57], v[2:3], off
	global_load_dwordx4 v[34:37], v[6:7], off
	v_add_u32_e32 v2, s27, v4
	v_mov_b32_e32 v3, v131
	v_lshl_add_u64 v[4:5], v[2:3], 2, s[18:19]
	v_add_u32_e32 v2, s27, v2
	v_lshl_add_u64 v[4:5], v[4:5], 0, s[6:7]
	v_lshl_add_u64 v[6:7], v[2:3], 2, s[18:19]
	v_mad_u64_u32 v[2:3], s[2:3], s27, 25, v[2:3]
	v_lshl_add_u64 v[4:5], v[4:5], 0, v[130:131]
	v_lshl_add_u64 v[6:7], v[6:7], 0, s[6:7]
	v_mov_b32_e32 v3, v131
	v_lshl_add_u64 v[6:7], v[6:7], 0, v[130:131]
	global_load_dwordx4 v[38:41], v[4:5], off
	global_load_dwordx4 v[46:49], v[6:7], off
	v_lshl_add_u64 v[4:5], v[2:3], 2, s[18:19]
	v_add_u32_e32 v12, s27, v2
	v_mov_b32_e32 v13, v131
	v_lshl_add_u64 v[4:5], v[4:5], 0, s[6:7]
	v_lshl_add_u64 v[2:3], v[12:13], 2, s[18:19]
	v_lshl_add_u64 v[10:11], v[4:5], 0, v[130:131]
	v_lshl_add_u64 v[2:3], v[2:3], 0, s[6:7]
	v_lshl_add_u64 v[14:15], v[2:3], 0, v[130:131]
	global_load_dwordx4 v[2:5], v[10:11], off
	global_load_dwordx4 v[6:9], v[14:15], off
	v_add_u32_e32 v10, s27, v12
	v_mov_b32_e32 v11, v131
	v_lshl_add_u64 v[12:13], v[10:11], 2, s[18:19]
	v_add_u32_e32 v20, s27, v10
	v_mov_b32_e32 v21, v131
	v_lshl_add_u64 v[12:13], v[12:13], 0, s[6:7]
	v_lshl_add_u64 v[10:11], v[20:21], 2, s[18:19]
	v_lshl_add_u64 v[18:19], v[12:13], 0, v[130:131]
	v_lshl_add_u64 v[10:11], v[10:11], 0, s[6:7]
	v_lshl_add_u64 v[22:23], v[10:11], 0, v[130:131]
	global_load_dwordx4 v[10:13], v[18:19], off
	global_load_dwordx4 v[14:17], v[22:23], off
	v_add_u32_e32 v18, s27, v20
	v_mov_b32_e32 v19, v131
	v_lshl_add_u64 v[20:21], v[18:19], 2, s[18:19]
	v_add_u32_e32 v28, s27, v18
	v_mov_b32_e32 v29, v131
	v_lshl_add_u64 v[20:21], v[20:21], 0, s[6:7]
	v_lshl_add_u64 v[18:19], v[28:29], 2, s[18:19]
	v_lshl_add_u64 v[26:27], v[20:21], 0, v[130:131]
	v_lshl_add_u64 v[18:19], v[18:19], 0, s[6:7]
	v_lshl_add_u64 v[30:31], v[18:19], 0, v[130:131]
	global_load_dwordx4 v[18:21], v[26:27], off
	global_load_dwordx4 v[22:25], v[30:31], off
	v_add_u32_e32 v26, s27, v28
	v_mov_b32_e32 v27, v131
	v_lshl_add_u64 v[28:29], v[26:27], 2, s[18:19]
	v_add_u32_e32 v26, s27, v26
	v_lshl_add_u64 v[28:29], v[28:29], 0, s[6:7]
	v_lshl_add_u64 v[26:27], v[26:27], 2, s[18:19]
	v_lshl_add_u64 v[68:69], v[28:29], 0, v[130:131]
	v_lshl_add_u64 v[26:27], v[26:27], 0, s[6:7]
	v_lshl_add_u64 v[70:71], v[26:27], 0, v[130:131]
	global_load_dwordx4 v[26:29], v[68:69], off
	global_load_dwordx4 v[30:33], v[70:71], off
	v_bfe_u32 v200, v67, 3, 3
	v_lshlrev_b32_e32 v70, 1, v67
	v_lshlrev_b32_e32 v75, 7, v200
	v_bfe_u32 v68, v67, 4, 2
	v_and_b32_e32 v71, 14, v70
	v_and_b32_e32 v76, 0x80, v75
	v_or_b32_e32 v90, 8, v200
	v_bitop3_b32 v70, v70, v68, 14 bitop3:0x6c
	v_bitop3_b32 v73, v68, v71, 4 bitop3:0x36
	v_bitop3_b32 v74, v68, v71, 8 bitop3:0x36
	v_bitop3_b32 v71, v68, v71, 12 bitop3:0x36
	v_or_b32_e32 v91, 16, v200
	v_or_b32_e32 v201, v76, v68
	v_lshrrev_b32_e32 v68, 1, v90
	v_or_b32_e32 v203, 24, v200
	v_or_b32_e32 v202, v68, v76
	v_lshrrev_b32_e32 v68, 1, v91
	v_or_b32_e32 v92, 32, v200
	v_or_b32_e32 v210, v68, v76
	v_lshrrev_b32_e32 v68, 1, v203
	v_or_b32_e32 v205, 40, v200
	v_or_b32_e32 v211, v68, v76
	v_lshrrev_b32_e32 v68, 1, v92
	v_or_b32_e32 v228, 48, v200
	v_or_b32_e32 v212, v68, v76
	v_lshrrev_b32_e32 v68, 1, v205
	v_or_b32_e32 v232, 56, v200
	v_or_b32_e32 v213, v68, v76
	v_lshrrev_b32_e32 v68, 1, v228
	v_or_b32_e32 v214, v68, v76
	v_lshrrev_b32_e32 v68, 1, v232
	v_or_b32_e32 v215, v68, v76
	v_or_b32_e32 v68, 64, v200
	v_lshrrev_b32_e32 v68, 1, v68
	v_or_b32_e32 v217, v68, v76
	v_or_b32_e32 v68, 0x48, v200
	v_lshrrev_b32_e32 v68, 1, v68
	v_or_b32_e32 v219, v68, v76
	v_or_b32_e32 v68, 0x50, v200
	v_lshrrev_b32_e32 v68, 1, v68
	v_or_b32_e32 v221, v68, v76
	v_or_b32_e32 v68, 0x58, v200
	v_lshrrev_b32_e32 v68, 1, v68
	v_or_b32_e32 v223, v68, v76
	v_or_b32_e32 v68, 0x60, v200
	v_lshrrev_b32_e32 v68, 1, v68
	v_or_b32_e32 v225, v68, v76
	v_or_b32_e32 v68, 0x68, v200
	v_lshrrev_b32_e32 v68, 1, v68
	v_or_b32_e32 v227, v68, v76
	v_or_b32_e32 v68, 0x70, v200
	v_lshrrev_b32_e32 v68, 1, v68
	v_or_b32_e32 v229, v68, v76
	v_or_b32_e32 v68, 0x78, v200
	v_lshrrev_b32_e32 v68, 1, v68
	v_or_b32_e32 v231, v68, v76
	v_or_b32_e32 v68, 0x80, v200
	v_lshrrev_b32_e32 v68, 1, v68
	v_or_b32_e32 v233, v68, v76
	v_or_b32_e32 v68, 0x88, v200
	v_lshrrev_b32_e32 v68, 1, v68
	v_or_b32_e32 v235, v68, v76
	v_or_b32_e32 v68, 0x90, v200
	v_lshrrev_b32_e32 v68, 1, v68
	v_or_b32_e32 v237, v68, v76
	v_or_b32_e32 v68, 0x98, v200
	v_lshrrev_b32_e32 v68, 1, v68
	v_or_b32_e32 v239, v68, v76
	v_or_b32_e32 v68, 0xa0, v200
	v_lshrrev_b32_e32 v68, 1, v68
	v_or_b32_e32 v241, v68, v76
	v_or_b32_e32 v68, 0xa8, v200
	v_lshrrev_b32_e32 v68, 1, v68
	v_or_b32_e32 v243, v68, v76
	v_or_b32_e32 v68, 0xb0, v200
	v_lshrrev_b32_e32 v68, 1, v68
	v_or_b32_e32 v245, v68, v76
	v_or_b32_e32 v68, 0xb8, v200
	v_lshrrev_b32_e32 v68, 1, v68
	v_or_b32_e32 v247, v68, v76
	v_or_b32_e32 v68, 0xc0, v200
	v_lshrrev_b32_e32 v68, 1, v68
	v_or_b32_e32 v249, v68, v76
	v_or_b32_e32 v68, 0xc8, v200
	v_lshrrev_b32_e32 v68, 1, v68
	v_or_b32_e32 v251, v68, v76
	v_or_b32_e32 v68, 0xd0, v200
	v_lshrrev_b32_e32 v68, 1, v68
	v_or_b32_e32 v253, v68, v76
	v_or_b32_e32 v68, 0xd8, v200
	v_lshrrev_b32_e32 v68, 1, v68
	v_or_b32_e32 v218, v68, v76
	v_or_b32_e32 v68, 0xe0, v200
	s_lshl_b32 s0, s0, 7
	v_lshrrev_b32_e32 v68, 1, v68
	s_and_b32 s0, s0, 0xffffe000
	v_or_b32_e32 v222, v68, v76
	v_or_b32_e32 v68, 0xe8, v200
	s_add_i32 s0, s0, 0
	v_lshlrev_b32_e32 v69, 9, v67
	v_lshrrev_b32_e32 v68, 1, v68
	v_and_b32_e32 v72, 63, v67
	s_add_i32 s0, s0, 0x10000
	v_and_b32_e32 v69, 0x1e00, v69
	v_or_b32_e32 v226, v68, v76
	v_or_b32_e32 v68, 0xf0, v200
	v_add_u32_e32 v69, s0, v69
	v_lshlrev_b32_e32 v72, 4, v72
	s_movk_i32 s1, 0x70
	v_add_u32_e32 v75, s0, v75
	v_bfe_u32 v67, v67, 1, 5
	v_lshl_add_u32 v77, v90, 7, s0
	v_lshlrev_b32_e32 v78, 2, v90
	v_lshl_add_u32 v79, v91, 7, s0
	v_lshlrev_b32_e32 v80, 2, v91
	v_lshl_add_u32 v81, v203, 7, s0
	v_lshlrev_b32_e32 v82, 2, v203
	v_lshl_add_u32 v83, v92, 7, s0
	v_lshl_add_u32 v84, v205, 7, s0
	v_lshlrev_b32_e32 v85, 2, v205
	v_lshl_add_u32 v86, v228, 7, s0
	v_lshlrev_b32_e32 v87, 2, v228
	v_lshl_add_u32 v88, v232, 7, s0
	v_lshlrev_b32_e32 v89, 2, v232
	v_lshrrev_b32_e32 v68, 1, v68
	s_add_u32 s0, s68, 0x7e000000
	v_and_b32_e32 v132, 0x70, v72
	v_bitop3_b32 v67, v67, s1, v72 bitop3:0x48
	v_bitop3_b32 v78, v78, s1, v72 bitop3:0x48
	v_bitop3_b32 v80, v80, s1, v72 bitop3:0x48
	v_bitop3_b32 v82, v82, s1, v72 bitop3:0x48
	v_bitop3_b32 v85, v85, s1, v72 bitop3:0x48
	v_bitop3_b32 v87, v87, s1, v72 bitop3:0x48
	v_bitop3_b32 v72, v89, s1, v72 bitop3:0x48
	v_or_b32_e32 v230, v68, v76
	v_or_b32_e32 v68, 0xf8, v200
	s_addc_u32 s1, s69, 0
	v_lshlrev_b32_e32 v70, 3, v70
	v_lshlrev_b32_e32 v73, 3, v73
	v_lshlrev_b32_e32 v74, 3, v74
	v_lshlrev_b32_e32 v71, 3, v71
	v_lshrrev_b32_e32 v68, 1, v68
	s_add_u32 s2, s68, 0x5e000000
	v_mov_b32_e32 v133, v131
	v_or_b32_e32 v234, v68, v76
	s_addc_u32 s3, s69, 0
	v_lshlrev_b32_e32 v130, 2, v66
	v_add_u32_e32 v236, v69, v70
	v_add_u32_e32 v238, v69, v73
	v_add_u32_e32 v240, v69, v74
	v_add_u32_e32 v242, v69, v71
	v_add_u32_e32 v244, v75, v67
	v_add_u32_e32 v246, v77, v78
	v_add_u32_e32 v248, v79, v80
	v_add_u32_e32 v250, v81, v82
	v_add_u32_e32 v252, v83, v67
	v_add_u32_e32 v204, v84, v85
	v_add_u32_e32 v216, v86, v87
	v_add_u32_e32 v220, v88, v72
	s_branch .LBB0_171
.LBB0_170:
	s_waitcnt vmcnt(11)
	v_mul_f32_e32 v106, 0x42800000, v106
	s_waitcnt vmcnt(10)
	v_mul_f32_e32 v110, 0x42800000, v110
	v_mov_b32_e32 v137, v131
	v_cvt_pk_fp8_f32 v137, v106, v110
	s_waitcnt vmcnt(9)
	v_mul_f32_e32 v98, 0x42800000, v98
	s_waitcnt vmcnt(8)
	v_mul_f32_e32 v102, 0x42800000, v102
	v_mov_b32_e32 v106, v131
	v_cvt_pk_fp8_f32 v137, v98, v102 op_sel:[0,0,1]
	v_mul_f32_e32 v98, 0x42800000, v115
	v_mul_f32_e32 v102, 0x42800000, v119
	v_cvt_pk_fp8_f32 v106, v98, v102
	v_mul_f32_e32 v98, 0x42800000, v107
	v_mul_f32_e32 v102, 0x42800000, v111
	v_mov_b32_e32 v107, v131
	v_cvt_pk_fp8_f32 v107, v98, v102
	v_mul_f32_e32 v98, 0x42800000, v99
	v_mul_f32_e32 v99, 0x42800000, v103
	v_mul_f32_e32 v102, 0x42800000, v120
	v_cvt_pk_fp8_f32 v107, v98, v99 op_sel:[0,0,1]
	v_mul_f32_e32 v99, 0x42800000, v116
	v_mov_b32_e32 v98, v131
	v_cvt_pk_fp8_f32 v98, v99, v102
	v_mul_f32_e32 v102, 0x42800000, v108
	v_mul_f32_e32 v108, 0x42800000, v112
	v_mov_b32_e32 v99, v131
	v_cvt_pk_fp8_f32 v99, v102, v108
	v_mul_f32_e32 v114, 0x42800000, v114
	v_mul_f32_e32 v118, 0x42800000, v118
	v_mov_b32_e32 v136, v131
	v_cvt_pk_fp8_f32 v136, v114, v118
	v_mul_f32_e32 v110, 0x42800000, v123
	v_mul_f32_e32 v114, 0x42800000, v127
	v_cvt_pk_fp8_f32 v106, v110, v114 op_sel:[0,0,1]
	v_mul_f32_e32 v103, 0x42800000, v124
	v_mul_f32_e32 v110, 0x42800000, v128
	v_mul_f32_e32 v100, 0x42800000, v100
	v_mul_f32_e32 v102, 0x42800000, v104
	v_cvt_pk_fp8_f32 v98, v103, v110 op_sel:[0,0,1]
	v_cvt_pk_fp8_f32 v99, v100, v102 op_sel:[0,0,1]
	v_mul_f32_e32 v100, 0x42800000, v117
	v_mul_f32_e32 v103, 0x42800000, v121
	v_mov_b32_e32 v102, v131
	v_cvt_pk_fp8_f32 v102, v100, v103
	v_mul_f32_e32 v100, 0x42800000, v109
	v_mul_f32_e32 v109, 0x42800000, v113
	v_mov_b32_e32 v103, v131
	v_cvt_pk_fp8_f32 v103, v100, v109
	v_mul_f32_e32 v100, 0x42800000, v101
	v_mul_f32_e32 v101, 0x42800000, v105
	s_waitcnt vmcnt(3)
	v_mul_f32_e32 v66, 0x42800000, v66
	v_cvt_pk_fp8_f32 v103, v100, v101 op_sel:[0,0,1]
	s_waitcnt vmcnt(2)
	v_mul_f32_e32 v70, 0x42800000, v70
	v_mov_b32_e32 v101, v131
	v_cvt_pk_fp8_f32 v101, v66, v70
	v_mul_f32_e32 v74, 0x42800000, v74
	v_mul_f32_e32 v78, 0x42800000, v78
	v_mov_b32_e32 v100, v131
	s_waitcnt vmcnt(1)
	v_mul_f32_e32 v66, 0x42800000, v90
	s_waitcnt vmcnt(0)
	v_mul_f32_e32 v70, 0x42800000, v94
	v_cvt_pk_fp8_f32 v100, v74, v78
	v_cvt_pk_fp8_f32 v101, v66, v70 op_sel:[0,0,1]
	v_mul_f32_e32 v70, 0x42800000, v75
	v_mul_f32_e32 v74, 0x42800000, v79
	v_mov_b32_e32 v66, v131
	v_cvt_pk_fp8_f32 v66, v70, v74
	v_mul_f32_e32 v70, 0x42800000, v67
	v_mul_f32_e32 v71, 0x42800000, v71
	v_mov_b32_e32 v67, v131
	v_cvt_pk_fp8_f32 v67, v70, v71
	v_mul_f32_e32 v70, 0x42800000, v91
	v_mul_f32_e32 v71, 0x42800000, v95
	v_mul_f32_e32 v74, 0x42800000, v80
	v_cvt_pk_fp8_f32 v67, v70, v71 op_sel:[0,0,1]
	v_mul_f32_e32 v71, 0x42800000, v76
	v_mov_b32_e32 v70, v131
	v_cvt_pk_fp8_f32 v70, v71, v74
	v_mul_f32_e32 v68, 0x42800000, v68
	v_mul_f32_e32 v72, 0x42800000, v72
	v_mov_b32_e32 v71, v131
	v_cvt_pk_fp8_f32 v71, v68, v72
	v_mul_f32_e32 v68, 0x42800000, v92
	v_mul_f32_e32 v72, 0x42800000, v96
	v_mul_f32_e32 v74, 0x42800000, v81
	v_cvt_pk_fp8_f32 v71, v68, v72 op_sel:[0,0,1]
	v_mul_f32_e32 v72, 0x42800000, v77
	v_mov_b32_e32 v68, v131
	v_cvt_pk_fp8_f32 v68, v72, v74
	v_mul_f32_e32 v72, 0x42800000, v69
	v_mul_f32_e32 v73, 0x42800000, v73
	v_mov_b32_e32 v69, v131
	v_mul_f32_e32 v122, 0x42800000, v122
	v_mul_f32_e32 v126, 0x42800000, v126
	v_cvt_pk_fp8_f32 v69, v72, v73
	v_cvt_pk_fp8_f32 v136, v122, v126 op_sel:[0,0,1]
	v_mul_f32_e32 v104, 0x42800000, v125
	v_mul_f32_e32 v108, 0x42800000, v129
	v_mul_f32_e32 v75, 0x42800000, v83
	v_mul_f32_e32 v78, 0x42800000, v87
	v_cvt_pk_fp8_f32 v102, v104, v108 op_sel:[0,0,1]
	v_mul_f32_e32 v82, 0x42800000, v82
	v_mul_f32_e32 v86, 0x42800000, v86
	v_cvt_pk_fp8_f32 v66, v75, v78 op_sel:[0,0,1]
	v_mul_f32_e32 v75, 0x42800000, v84
	v_mul_f32_e32 v76, 0x42800000, v88
	v_cvt_pk_fp8_f32 v100, v82, v86 op_sel:[0,0,1]
	v_cvt_pk_fp8_f32 v70, v75, v76 op_sel:[0,0,1]
	v_mul_f32_e32 v75, 0x42800000, v85
	v_mul_f32_e32 v76, 0x42800000, v89
	v_mul_f32_e32 v72, 0x42800000, v93
	v_mul_f32_e32 v73, 0x42800000, v97
	v_cvt_pk_fp8_f32 v68, v75, v76 op_sel:[0,0,1]
	v_cvt_pk_fp8_f32 v69, v72, v73 op_sel:[0,0,1]
	ds_write2_b64 v240, v[136:137], v[106:107] offset1:16
	ds_write2_b64 v240, v[98:99], v[102:103] offset0:32 offset1:48
	ds_write2_b64 v242, v[100:101], v[66:67] offset1:16
	ds_write2_b64 v242, v[70:71], v[68:69] offset0:32 offset1:48
	ds_read_b128 v[66:69], v244
	v_or_b32_e32 v70, 0xc0, v200
	v_cndmask_b32_e64 v70, v249, v70, s[6:7]
	v_or_b32_e32 v70, s8, v70
	v_mov_b32_e32 v71, v131
	v_lshlrev_b64 v[70:71], 11, v[70:71]
	v_lshl_add_u64 v[74:75], v[134:135], 0, v[70:71]
	ds_read_b128 v[70:73], v246
	s_waitcnt lgkmcnt(1)
	global_store_dwordx4 v[74:75], v[66:69], off
	v_readfirstlane_b32 s22, v224
	s_andn2_b64 vcc, exec, s[10:11]
	v_or_b32_e32 v66, 0xc8, v200
	v_cndmask_b32_e64 v66, v251, v66, s[6:7]
	v_or_b32_e32 v66, s8, v66
	v_mov_b32_e32 v67, v131
	v_lshlrev_b64 v[66:67], 11, v[66:67]
	v_lshl_add_u64 v[66:67], v[134:135], 0, v[66:67]
	s_waitcnt lgkmcnt(0)
	global_store_dwordx4 v[66:67], v[70:73], off
	ds_read_b128 v[66:69], v248
	s_mov_b64 s[18:19], s[12:13]
	v_or_b32_e32 v70, 0xd0, v200
	v_cndmask_b32_e64 v70, v253, v70, s[6:7]
	v_or_b32_e32 v70, s8, v70
	v_mov_b32_e32 v71, v131
	v_lshlrev_b64 v[70:71], 11, v[70:71]
	v_lshl_add_u64 v[74:75], v[134:135], 0, v[70:71]
	ds_read_b128 v[70:73], v250
	s_waitcnt lgkmcnt(1)
	global_store_dwordx4 v[74:75], v[66:69], off
	s_mov_b64 s[20:21], s[14:15]
	s_mov_b32 s27, s26
	v_or_b32_e32 v66, 0xd8, v200
	v_cndmask_b32_e64 v66, v218, v66, s[6:7]
	v_or_b32_e32 v66, s8, v66
	v_mov_b32_e32 v67, v131
	v_lshlrev_b64 v[66:67], 11, v[66:67]
	v_lshl_add_u64 v[66:67], v[134:135], 0, v[66:67]
	s_waitcnt lgkmcnt(0)
	global_store_dwordx4 v[66:67], v[70:73], off
	ds_read_b128 v[66:69], v252
	s_mov_b32 s30, s4
	v_or_b32_e32 v70, 0xe0, v200
	v_cndmask_b32_e64 v70, v222, v70, s[6:7]
	v_or_b32_e32 v70, s8, v70
	v_mov_b32_e32 v71, v131
	v_lshlrev_b64 v[70:71], 11, v[70:71]
	v_lshl_add_u64 v[74:75], v[134:135], 0, v[70:71]
	ds_read_b128 v[70:73], v204
	s_waitcnt lgkmcnt(1)
	global_store_dwordx4 v[74:75], v[66:69], off
	s_mov_b32 s29, s24
	s_mov_b32 s28, s25
	v_or_b32_e32 v66, 0xe8, v200
	v_cndmask_b32_e64 v66, v226, v66, s[6:7]
	v_or_b32_e32 v66, s8, v66
	v_mov_b32_e32 v67, v131
	v_lshlrev_b64 v[66:67], 11, v[66:67]
	v_lshl_add_u64 v[66:67], v[134:135], 0, v[66:67]
	s_waitcnt lgkmcnt(0)
	global_store_dwordx4 v[66:67], v[70:73], off
	ds_read_b128 v[66:69], v216
	s_nop 0
	v_or_b32_e32 v70, 0xf0, v200
	v_cndmask_b32_e64 v70, v230, v70, s[6:7]
	v_or_b32_e32 v70, s8, v70
	v_mov_b32_e32 v71, v131
	v_lshlrev_b64 v[70:71], 11, v[70:71]
	v_lshl_add_u64 v[74:75], v[134:135], 0, v[70:71]
	ds_read_b128 v[70:73], v220
	s_waitcnt lgkmcnt(1)
	global_store_dwordx4 v[74:75], v[66:69], off
	s_nop 1
	v_or_b32_e32 v66, 0xf8, v200
	v_cndmask_b32_e64 v66, v234, v66, s[6:7]
	v_or_b32_e32 v66, s8, v66
	v_mov_b32_e32 v67, v131
	v_lshlrev_b64 v[66:67], 11, v[66:67]
	v_lshl_add_u64 v[66:67], v[134:135], 0, v[66:67]
	s_waitcnt lgkmcnt(0)
	global_store_dwordx4 v[66:67], v[70:73], off
	s_cbranch_vccz .LBB0_182

.LBB0_180:
	s_or_b64 exec, exec, s[4:5]
	s_lshl_b32 s5, s30, 7
	v_or_b32_e32 v84, s5, v1
	v_or_b32_e32 v82, 0x60, v84
	v_mad_u64_u32 v[82:83], s[6:7], v82, s27, 0
	v_lshl_add_u64 v[82:83], v[82:83], 2, s[18:19]
	v_lshl_add_u64 v[152:153], v[82:83], 0, v[130:131]
	v_or_b32_e32 v82, 0x61, v84
	v_mad_u64_u32 v[82:83], s[6:7], v82, s27, 0
	v_lshl_add_u64 v[82:83], v[82:83], 2, s[18:19]
	v_lshl_add_u64 v[154:155], v[82:83], 0, v[130:131]
	v_or_b32_e32 v82, 0x62, v84
	v_mad_u64_u32 v[82:83], s[6:7], v82, s27, 0
	v_lshl_add_u64 v[82:83], v[82:83], 2, s[18:19]
	v_lshl_add_u64 v[156:157], v[82:83], 0, v[130:131]
	v_or_b32_e32 v82, 0x63, v84
	v_mad_u64_u32 v[82:83], s[6:7], v82, s27, 0
	v_lshl_add_u64 v[82:83], v[82:83], 2, s[18:19]
	v_lshl_add_u64 v[158:159], v[82:83], 0, v[130:131]
	v_or_b32_e32 v82, 0x64, v84
	v_mad_u64_u32 v[82:83], s[6:7], v82, s27, 0
	v_lshl_add_u64 v[82:83], v[82:83], 2, s[18:19]
	v_lshl_add_u64 v[160:161], v[82:83], 0, v[130:131]
	v_or_b32_e32 v82, 0x65, v84
	v_mad_u64_u32 v[82:83], s[6:7], v82, s27, 0
	v_lshl_add_u64 v[82:83], v[82:83], 2, s[18:19]
	v_lshl_add_u64 v[162:163], v[82:83], 0, v[130:131]
	v_or_b32_e32 v82, 0x66, v84
	v_mad_u64_u32 v[82:83], s[6:7], v82, s27, 0
	v_lshl_add_u64 v[82:83], v[82:83], 2, s[18:19]
	s_and_b32 s4, s8, 15
	s_lshl_b32 s8, s29, 8
	v_or_b32_e32 v66, 64, v84
	v_or_b32_e32 v68, 0x41, v84
	v_or_b32_e32 v70, 0x42, v84
	v_or_b32_e32 v72, 0x43, v84
	v_or_b32_e32 v74, 0x44, v84
	v_or_b32_e32 v76, 0x45, v84
	v_or_b32_e32 v78, 0x46, v84
	v_or_b32_e32 v80, 0x47, v84
	v_lshl_add_u64 v[106:107], v[82:83], 0, v[130:131]
	v_or_b32_e32 v82, 0x67, v84
	v_mad_u64_u32 v[66:67], s[6:7], v66, s27, 0
	v_mad_u64_u32 v[68:69], s[6:7], v68, s27, 0
	v_mad_u64_u32 v[70:71], s[6:7], v70, s27, 0
	v_mad_u64_u32 v[72:73], s[6:7], v72, s27, 0
	v_mad_u64_u32 v[74:75], s[6:7], v74, s27, 0
	v_mad_u64_u32 v[76:77], s[6:7], v76, s27, 0
	v_mad_u64_u32 v[78:79], s[6:7], v78, s27, 0
	v_mad_u64_u32 v[80:81], s[6:7], v80, s27, 0
	v_mad_u64_u32 v[82:83], s[6:7], v82, s27, 0
	s_cmp_eq_u32 s28, 0
	s_cselect_b64 s[6:7], -1, 0
	s_add_u32 s20, s20, s5
	v_lshl_add_u64 v[82:83], v[82:83], 2, s[18:19]
	s_addc_u32 s21, s21, 0
	v_lshl_add_u64 v[108:109], v[82:83], 0, v[130:131]
	v_lshl_add_u64 v[134:135], s[20:21], 0, v[132:133]
	v_mad_u64_u32 v[82:83], s[20:21], v84, s27, 0
	v_lshl_add_u64 v[82:83], v[82:83], 2, s[18:19]
	v_lshl_add_u64 v[110:111], v[82:83], 0, v[130:131]
	v_or_b32_e32 v82, 1, v84
	v_mad_u64_u32 v[82:83], s[20:21], v82, s27, 0
	v_lshl_add_u64 v[82:83], v[82:83], 2, s[18:19]
	v_lshl_add_u64 v[112:113], v[82:83], 0, v[130:131]
	v_or_b32_e32 v82, 2, v84
	v_mad_u64_u32 v[82:83], s[20:21], v82, s27, 0
	v_lshl_add_u64 v[82:83], v[82:83], 2, s[18:19]
	v_lshl_add_u64 v[114:115], v[82:83], 0, v[130:131]
	v_or_b32_e32 v82, 3, v84
	v_mad_u64_u32 v[82:83], s[20:21], v82, s27, 0
	v_lshl_add_u64 v[82:83], v[82:83], 2, s[18:19]
	v_lshl_add_u64 v[116:117], v[82:83], 0, v[130:131]
	v_or_b32_e32 v82, 4, v84
	v_mad_u64_u32 v[82:83], s[20:21], v82, s27, 0
	v_lshl_add_u64 v[82:83], v[82:83], 2, s[18:19]
	v_lshl_add_u64 v[118:119], v[82:83], 0, v[130:131]
	v_or_b32_e32 v82, 5, v84
	v_mad_u64_u32 v[82:83], s[20:21], v82, s27, 0
	v_lshl_add_u64 v[82:83], v[82:83], 2, s[18:19]
	v_lshl_add_u64 v[120:121], v[82:83], 0, v[130:131]
	v_or_b32_e32 v82, 6, v84
	v_mad_u64_u32 v[82:83], s[20:21], v82, s27, 0
	v_lshl_add_u64 v[82:83], v[82:83], 2, s[18:19]
	v_lshl_add_u64 v[122:123], v[82:83], 0, v[130:131]
	v_or_b32_e32 v82, 7, v84
	v_mad_u64_u32 v[82:83], s[20:21], v82, s27, 0
	v_lshl_add_u64 v[82:83], v[82:83], 2, s[18:19]
	v_lshl_add_u64 v[124:125], v[82:83], 0, v[130:131]
	v_or_b32_e32 v82, 32, v84
	v_mad_u64_u32 v[82:83], s[20:21], v82, s27, 0
	v_lshl_add_u64 v[82:83], v[82:83], 2, s[18:19]
	v_lshl_add_u64 v[126:127], v[82:83], 0, v[130:131]
	v_or_b32_e32 v82, 33, v84
	v_mad_u64_u32 v[82:83], s[20:21], v82, s27, 0
	v_lshl_add_u64 v[82:83], v[82:83], 2, s[18:19]
	v_lshl_add_u64 v[128:129], v[82:83], 0, v[130:131]
	v_or_b32_e32 v82, 34, v84
	v_mad_u64_u32 v[82:83], s[20:21], v82, s27, 0
	v_lshl_add_u64 v[82:83], v[82:83], 2, s[18:19]
	v_lshl_add_u64 v[178:179], v[82:83], 0, v[130:131]
	v_or_b32_e32 v82, 35, v84
	v_mad_u64_u32 v[82:83], s[20:21], v82, s27, 0
	v_lshl_add_u64 v[82:83], v[82:83], 2, s[18:19]
	v_lshl_add_u64 v[176:177], v[82:83], 0, v[130:131]
	v_or_b32_e32 v82, 36, v84
	v_mad_u64_u32 v[82:83], s[20:21], v82, s27, 0
	v_lshl_add_u64 v[82:83], v[82:83], 2, s[18:19]
	v_lshl_add_u64 v[174:175], v[82:83], 0, v[130:131]
	v_or_b32_e32 v82, 37, v84
	v_mad_u64_u32 v[82:83], s[20:21], v82, s27, 0
	v_lshl_add_u64 v[82:83], v[82:83], 2, s[18:19]
	v_lshl_add_u64 v[172:173], v[82:83], 0, v[130:131]
	v_or_b32_e32 v82, 38, v84
	v_mad_u64_u32 v[82:83], s[20:21], v82, s27, 0
	v_lshl_add_u64 v[82:83], v[82:83], 2, s[18:19]
	v_lshl_add_u64 v[170:171], v[82:83], 0, v[130:131]
	v_or_b32_e32 v82, 39, v84
	v_lshl_add_u64 v[66:67], v[66:67], 2, s[18:19]
	v_mad_u64_u32 v[82:83], s[20:21], v82, s27, 0
	v_lshl_add_u64 v[66:67], v[66:67], 0, v[130:131]
	v_lshl_add_u64 v[68:69], v[68:69], 2, s[18:19]
	v_lshl_add_u64 v[70:71], v[70:71], 2, s[18:19]
	v_lshl_add_u64 v[72:73], v[72:73], 2, s[18:19]
	v_lshl_add_u64 v[74:75], v[74:75], 2, s[18:19]
	v_lshl_add_u64 v[76:77], v[76:77], 2, s[18:19]
	v_lshl_add_u64 v[78:79], v[78:79], 2, s[18:19]
	v_lshl_add_u64 v[80:81], v[80:81], 2, s[18:19]
	v_lshl_add_u64 v[82:83], v[82:83], 2, s[18:19]
	s_lshl_b64 s[18:19], s[8:9], 2
	v_lshl_add_u64 v[68:69], v[68:69], 0, v[130:131]
	v_lshl_add_u64 v[70:71], v[70:71], 0, v[130:131]
	v_lshl_add_u64 v[74:75], v[74:75], 0, v[130:131]
	v_lshl_add_u64 v[136:137], v[66:67], 0, s[18:19]
	v_lshl_add_u64 v[72:73], v[72:73], 0, v[130:131]
	v_lshl_add_u64 v[76:77], v[76:77], 0, v[130:131]
	v_lshl_add_u64 v[138:139], v[68:69], 0, s[18:19]
	global_load_dwordx4 v[98:101], v[136:137], off
	global_load_dwordx4 v[102:105], v[138:139], off
	v_lshl_add_u64 v[140:141], v[70:71], 0, s[18:19]
	v_lshl_add_u64 v[144:145], v[74:75], 0, s[18:19]
	v_lshl_add_u64 v[168:169], v[82:83], 0, v[130:131]
	v_lshl_add_u64 v[142:143], v[72:73], 0, s[18:19]
	global_load_dwordx4 v[94:97], v[140:141], off
	global_load_dwordx4 v[90:93], v[142:143], off
	v_lshl_add_u64 v[146:147], v[76:77], 0, s[18:19]
	global_load_dwordx4 v[86:89], v[144:145], off
	global_load_dwordx4 v[82:85], v[146:147], off
	v_lshl_add_u64 v[78:79], v[78:79], 0, v[130:131]
	v_lshl_add_u64 v[80:81], v[80:81], 0, v[130:131]
	v_lshl_add_u64 v[148:149], v[78:79], 0, s[18:19]
	v_lshl_add_u64 v[150:151], v[80:81], 0, s[18:19]
	global_load_dwordx4 v[74:77], v[148:149], off
	global_load_dwordx4 v[78:81], v[150:151], off
	s_waitcnt vmcnt(23)
	v_mul_f32_e32 v181, 0x42800000, v58
	s_waitcnt vmcnt(22)
	v_mul_f32_e32 v182, 0x42800000, v62
	v_mov_b32_e32 v180, v131
	v_cvt_pk_fp8_f32 v180, v181, v182
	s_waitcnt vmcnt(19)
	v_mul_f32_e32 v54, 0x42800000, v54
	s_waitcnt vmcnt(18)
	v_mul_f32_e32 v34, 0x42800000, v34
	v_mov_b32_e32 v181, v131
	v_cvt_pk_fp8_f32 v181, v54, v34
	v_mul_f32_e32 v34, 0x42800000, v50
	v_mul_f32_e32 v42, 0x42800000, v42
	v_cvt_pk_fp8_f32 v180, v34, v42 op_sel:[0,0,1]
	s_waitcnt vmcnt(17)
	v_mul_f32_e32 v34, 0x42800000, v38
	s_waitcnt vmcnt(16)
	v_mul_f32_e32 v38, 0x42800000, v46
	v_mul_f32_e32 v183, 0x42800000, v59
	v_mul_f32_e32 v184, 0x42800000, v63
	v_cvt_pk_fp8_f32 v181, v34, v38 op_sel:[0,0,1]
	v_mov_b32_e32 v34, v131
	v_cvt_pk_fp8_f32 v34, v183, v184
	v_mul_f32_e32 v38, 0x42800000, v55
	v_mul_f32_e32 v42, 0x42800000, v35
	v_mov_b32_e32 v35, v131
	v_cvt_pk_fp8_f32 v35, v38, v42
	v_mul_f32_e32 v38, 0x42800000, v51
	v_mul_f32_e32 v42, 0x42800000, v43
	v_cvt_pk_fp8_f32 v34, v38, v42 op_sel:[0,0,1]
	v_mul_f32_e32 v38, 0x42800000, v39
	v_mul_f32_e32 v39, 0x42800000, v47
	v_lshl_add_u64 v[152:153], v[152:153], 0, s[18:19]
	v_cvt_pk_fp8_f32 v35, v38, v39 op_sel:[0,0,1]
	v_mul_f32_e32 v42, 0x42800000, v56
	v_mul_f32_e32 v36, 0x42800000, v36
	v_mov_b32_e32 v39, v131
	v_lshl_add_u64 v[154:155], v[154:155], 0, s[18:19]
	global_load_dwordx4 v[66:69], v[152:153], off
	global_load_dwordx4 v[70:73], v[154:155], off
	v_lshl_add_u64 v[156:157], v[156:157], 0, s[18:19]
	v_mul_f32_e32 v185, 0x42800000, v60
	v_mul_f32_e32 v186, 0x42800000, v64
	v_lshl_add_u64 v[164:165], v[160:161], 0, s[18:19]
	v_mov_b32_e32 v38, v131
	v_cvt_pk_fp8_f32 v39, v42, v36
	v_lshl_add_u64 v[158:159], v[158:159], 0, s[18:19]
	v_mul_f32_e32 v187, 0x42800000, v61
	v_mul_f32_e32 v188, 0x42800000, v65
	global_load_dwordx4 v[58:61], v[156:157], off
	global_load_dwordx4 v[62:65], v[158:159], off
	v_lshl_add_u64 v[166:167], v[162:163], 0, s[18:19]
	v_mul_f32_e32 v46, 0x42800000, v52
	v_mul_f32_e32 v47, 0x42800000, v53
	v_mul_f32_e32 v54, 0x42800000, v44
	v_mul_f32_e32 v182, 0x42800000, v45
	v_cvt_pk_fp8_f32 v38, v185, v186
	global_load_dwordx4 v[42:45], v[164:165], off
	global_load_dwordx4 v[50:53], v[166:167], off
	v_mul_f32_e32 v56, 0x42800000, v37
	v_mul_f32_e32 v36, 0x42800000, v40
	v_mul_f32_e32 v37, 0x42800000, v48
	v_mul_f32_e32 v55, 0x42800000, v57
	v_lshl_add_u64 v[160:161], v[106:107], 0, s[18:19]
	v_cvt_pk_fp8_f32 v39, v36, v37 op_sel:[0,0,1]
	v_mov_b32_e32 v37, v131
	v_lshl_add_u64 v[162:163], v[108:109], 0, s[18:19]
	v_cvt_pk_fp8_f32 v38, v46, v54 op_sel:[0,0,1]
	v_cvt_pk_fp8_f32 v37, v55, v56
	global_load_dwordx4 v[54:57], v[160:161], off
	global_load_dwordx4 v[106:109], v[162:163], off
	v_mov_b32_e32 v36, v131
	v_cvt_pk_fp8_f32 v36, v187, v188
	v_mul_f32_e32 v40, 0x42800000, v41
	v_mul_f32_e32 v41, 0x42800000, v49
	v_cvt_pk_fp8_f32 v37, v40, v41 op_sel:[0,0,1]
	v_cvt_pk_fp8_f32 v36, v47, v182 op_sel:[0,0,1]
	ds_write_b64 v236, v[180:181]
	ds_write_b64 v236, v[34:35] offset:128
	ds_write_b64 v236, v[38:39] offset:256
	ds_write_b64 v236, v[36:37] offset:384
	s_waitcnt vmcnt(23)
	v_mul_f32_e32 v2, 0x42800000, v2
	s_waitcnt vmcnt(22)
	v_mul_f32_e32 v6, 0x42800000, v6
	v_mov_b32_e32 v34, v131
	v_cvt_pk_fp8_f32 v34, v2, v6
	s_waitcnt vmcnt(19)
	v_mul_f32_e32 v2, 0x42800000, v18
	s_waitcnt vmcnt(18)
	v_mul_f32_e32 v6, 0x42800000, v22
	v_mov_b32_e32 v35, v131
	v_cvt_pk_fp8_f32 v35, v2, v6
	s_waitcnt vmcnt(17)
	v_mul_f32_e32 v2, 0x42800000, v26
	s_waitcnt vmcnt(16)
	v_mul_f32_e32 v6, 0x42800000, v30
	v_mul_f32_e32 v3, 0x42800000, v3
	v_cvt_pk_fp8_f32 v35, v2, v6 op_sel:[0,0,1]
	v_mul_f32_e32 v6, 0x42800000, v7
	v_mov_b32_e32 v2, v131
	v_mul_f32_e32 v7, 0x42800000, v11
	v_cvt_pk_fp8_f32 v2, v3, v6
	v_mul_f32_e32 v6, 0x42800000, v19
	v_mul_f32_e32 v11, 0x42800000, v23
	v_mov_b32_e32 v3, v131
	v_cvt_pk_fp8_f32 v3, v6, v11
	v_mul_f32_e32 v10, 0x42800000, v10
	v_mul_f32_e32 v14, 0x42800000, v14
	v_cvt_pk_fp8_f32 v34, v10, v14 op_sel:[0,0,1]
	v_mul_f32_e32 v10, 0x42800000, v15
	v_cvt_pk_fp8_f32 v2, v7, v10 op_sel:[0,0,1]
	v_mul_f32_e32 v6, 0x42800000, v27
	v_mul_f32_e32 v7, 0x42800000, v31
	v_cvt_pk_fp8_f32 v3, v6, v7 op_sel:[0,0,1]
	v_mul_f32_e32 v4, 0x42800000, v4
	v_mul_f32_e32 v7, 0x42800000, v8
	v_mov_b32_e32 v6, v131
	s_waitcnt vmcnt(15)
	v_mul_f32_e32 v47, 0x42800000, v98
	s_waitcnt vmcnt(14)
	v_mul_f32_e32 v48, 0x42800000, v102
	v_mov_b32_e32 v46, v131
	v_cvt_pk_fp8_f32 v6, v4, v7
	v_mul_f32_e32 v4, 0x42800000, v20
	v_mul_f32_e32 v11, 0x42800000, v24
	v_mov_b32_e32 v7, v131
	v_cvt_pk_fp8_f32 v46, v47, v48
	s_waitcnt vmcnt(11)
	v_mul_f32_e32 v48, 0x42800000, v86
	s_waitcnt vmcnt(10)
	v_mul_f32_e32 v82, 0x42800000, v82
	v_mov_b32_e32 v47, v131
	v_cvt_pk_fp8_f32 v7, v4, v11
	v_cvt_pk_fp8_f32 v47, v48, v82
	v_mul_f32_e32 v8, 0x42800000, v12
	v_mul_f32_e32 v10, 0x42800000, v16
	v_mul_f32_e32 v48, 0x42800000, v94
	v_mul_f32_e32 v82, 0x42800000, v90
	v_cvt_pk_fp8_f32 v6, v8, v10 op_sel:[0,0,1]
	v_mul_f32_e32 v4, 0x42800000, v28
	v_mul_f32_e32 v8, 0x42800000, v32
	v_cvt_pk_fp8_f32 v46, v48, v82 op_sel:[0,0,1]
	s_waitcnt vmcnt(9)
	v_mul_f32_e32 v48, 0x42800000, v74
	s_waitcnt vmcnt(8)
	v_mul_f32_e32 v74, 0x42800000, v78
	v_cvt_pk_fp8_f32 v7, v4, v8 op_sel:[0,0,1]
	v_mul_f32_e32 v5, 0x42800000, v5
	v_mul_f32_e32 v8, 0x42800000, v9
	v_mov_b32_e32 v4, v131
	v_lshl_add_u64 v[190:191], v[118:119], 0, s[18:19]
	v_mul_f32_e32 v49, 0x42800000, v99
	v_mul_f32_e32 v118, 0x42800000, v103
	v_cvt_pk_fp8_f32 v47, v48, v74 op_sel:[0,0,1]
	v_mov_b32_e32 v48, v131
	v_cvt_pk_fp8_f32 v4, v5, v8
	v_mul_f32_e32 v8, 0x42800000, v21
	v_mul_f32_e32 v11, 0x42800000, v25
	v_mov_b32_e32 v5, v131
	v_cvt_pk_fp8_f32 v48, v49, v118
	v_mul_f32_e32 v74, 0x42800000, v87
	v_mul_f32_e32 v78, 0x42800000, v83
	v_mov_b32_e32 v49, v131
	v_cvt_pk_fp8_f32 v5, v8, v11
	v_cvt_pk_fp8_f32 v49, v74, v78
	v_mul_f32_e32 v9, 0x42800000, v13
	v_mul_f32_e32 v10, 0x42800000, v17
	v_mul_f32_e32 v74, 0x42800000, v95
	v_mul_f32_e32 v78, 0x42800000, v91
	v_cvt_pk_fp8_f32 v4, v9, v10 op_sel:[0,0,1]
	v_mul_f32_e32 v8, 0x42800000, v29
	v_mul_f32_e32 v9, 0x42800000, v33
	v_cvt_pk_fp8_f32 v48, v74, v78 op_sel:[0,0,1]
	v_mul_f32_e32 v74, 0x42800000, v75
	v_mul_f32_e32 v75, 0x42800000, v79
	v_cvt_pk_fp8_f32 v5, v8, v9 op_sel:[0,0,1]
	v_lshl_add_u64 v[188:189], v[120:121], 0, s[18:19]
	v_mul_f32_e32 v119, 0x42800000, v100
	v_mul_f32_e32 v120, 0x42800000, v104
	v_cvt_pk_fp8_f32 v49, v74, v75 op_sel:[0,0,1]
	v_mov_b32_e32 v74, v131
	ds_write_b64 v238, v[34:35]
	ds_write_b64 v238, v[2:3] offset:128
	ds_write_b64 v238, v[6:7] offset:256
	ds_write_b64 v238, v[4:5] offset:384
	v_lshl_add_u64 v[168:169], v[168:169], 0, s[18:19]
	v_lshl_add_u64 v[172:173], v[172:173], 0, s[18:19]
	v_lshl_add_u64 v[176:177], v[176:177], 0, s[18:19]
	v_lshl_add_u64 v[180:181], v[128:129], 0, s[18:19]
	v_lshl_add_u64 v[184:185], v[124:125], 0, s[18:19]
	v_lshl_add_u64 v[192:193], v[116:117], 0, s[18:19]
	v_cvt_pk_fp8_f32 v74, v119, v120
	v_mul_f32_e32 v86, 0x42800000, v88
	v_mul_f32_e32 v84, 0x42800000, v84
	v_mov_b32_e32 v75, v131
	v_lshl_add_u64 v[196:197], v[112:113], 0, s[18:19]
	v_lshl_add_u64 v[170:171], v[170:171], 0, s[18:19]
	global_load_dwordx4 v[2:5], v[168:169], off offset:256
	global_load_dwordx4 v[6:9], v[170:171], off offset:256
	v_lshl_add_u64 v[174:175], v[174:175], 0, s[18:19]
	global_load_dwordx4 v[10:13], v[172:173], off offset:256
	global_load_dwordx4 v[14:17], v[174:175], off offset:256
	v_lshl_add_u64 v[178:179], v[178:179], 0, s[18:19]
	global_load_dwordx4 v[18:21], v[176:177], off offset:256
	global_load_dwordx4 v[22:25], v[178:179], off offset:256
	v_lshl_add_u64 v[182:183], v[126:127], 0, s[18:19]
	global_load_dwordx4 v[26:29], v[180:181], off offset:256
	global_load_dwordx4 v[30:33], v[182:183], off offset:256
	v_lshl_add_u64 v[186:187], v[122:123], 0, s[18:19]
	global_load_dwordx4 v[34:37], v[184:185], off offset:256
	global_load_dwordx4 v[38:41], v[186:187], off offset:256
	v_mul_f32_e32 v121, 0x42800000, v101
	v_mul_f32_e32 v122, 0x42800000, v105
	global_load_dwordx4 v[98:101], v[188:189], off offset:256
	global_load_dwordx4 v[102:105], v[190:191], off offset:256
	v_lshl_add_u64 v[194:195], v[114:115], 0, s[18:19]
	v_mul_f32_e32 v79, 0x42800000, v92
	v_mul_f32_e32 v83, 0x42800000, v93
	v_cvt_pk_fp8_f32 v75, v86, v84
	v_mul_f32_e32 v84, 0x42800000, v89
	global_load_dwordx4 v[86:89], v[192:193], off offset:256
	global_load_dwordx4 v[90:93], v[194:195], off offset:256
	v_lshl_add_u64 v[198:199], v[110:111], 0, s[18:19]
	global_load_dwordx4 v[110:113], v[196:197], off offset:256
	global_load_dwordx4 v[114:117], v[198:199], off offset:256
	v_mul_f32_e32 v78, 0x42800000, v96
	v_cvt_pk_fp8_f32 v74, v78, v79 op_sel:[0,0,1]
	v_mul_f32_e32 v76, 0x42800000, v76
	v_mul_f32_e32 v78, 0x42800000, v80
	v_mul_f32_e32 v85, 0x42800000, v85
	v_cvt_pk_fp8_f32 v75, v76, v78 op_sel:[0,0,1]
	v_mov_b32_e32 v78, v131
	v_mov_b32_e32 v79, v131
	v_cvt_pk_fp8_f32 v78, v121, v122
	v_cvt_pk_fp8_f32 v79, v84, v85
	v_mul_f32_e32 v82, 0x42800000, v97
	v_mul_f32_e32 v76, 0x42800000, v77
	v_mul_f32_e32 v77, 0x42800000, v81
	v_cvt_pk_fp8_f32 v78, v82, v83 op_sel:[0,0,1]
	v_cvt_pk_fp8_f32 v79, v76, v77 op_sel:[0,0,1]
	ds_write_b64 v240, v[46:47]
	ds_write_b64 v240, v[48:49] offset:128
	ds_write_b64 v240, v[74:75] offset:256
	ds_write_b64 v240, v[78:79] offset:384
	s_waitcnt vmcnt(23)
	v_mul_f32_e32 v47, 0x42800000, v66
	s_waitcnt vmcnt(22)
	v_mul_f32_e32 v48, 0x42800000, v70
	v_mov_b32_e32 v46, v131
	v_cvt_pk_fp8_f32 v46, v47, v48
	s_waitcnt vmcnt(19)
	v_mul_f32_e32 v42, 0x42800000, v42
	s_waitcnt vmcnt(18)
	v_mul_f32_e32 v48, 0x42800000, v50
	v_mov_b32_e32 v47, v131
	v_cvt_pk_fp8_f32 v47, v42, v48
	v_mul_f32_e32 v49, 0x42800000, v58
	v_mul_f32_e32 v58, 0x42800000, v62
	s_waitcnt vmcnt(17)
	v_mul_f32_e32 v42, 0x42800000, v54
	s_waitcnt vmcnt(16)
	v_mul_f32_e32 v48, 0x42800000, v106
	v_cvt_pk_fp8_f32 v46, v49, v58 op_sel:[0,0,1]
	v_cvt_pk_fp8_f32 v47, v42, v48 op_sel:[0,0,1]
	v_mul_f32_e32 v48, 0x42800000, v67
	v_mul_f32_e32 v49, 0x42800000, v71
	v_mov_b32_e32 v42, v131
	v_cvt_pk_fp8_f32 v42, v48, v49
	v_mul_f32_e32 v48, 0x42800000, v43
	v_mul_f32_e32 v49, 0x42800000, v51
	v_mov_b32_e32 v43, v131
	v_cvt_pk_fp8_f32 v43, v48, v49
	v_mul_f32_e32 v50, 0x42800000, v59
	v_mul_f32_e32 v54, 0x42800000, v63
	v_mul_f32_e32 v48, 0x42800000, v55
	v_mul_f32_e32 v49, 0x42800000, v107
	v_cvt_pk_fp8_f32 v42, v50, v54 op_sel:[0,0,1]
	v_cvt_pk_fp8_f32 v43, v48, v49 op_sel:[0,0,1]
	v_mul_f32_e32 v49, 0x42800000, v68
	v_mul_f32_e32 v50, 0x42800000, v72
	v_mov_b32_e32 v48, v131
	v_cvt_pk_fp8_f32 v48, v49, v50
	v_mul_f32_e32 v44, 0x42800000, v44
	v_mul_f32_e32 v50, 0x42800000, v52
	v_mov_b32_e32 v49, v131
	v_cvt_pk_fp8_f32 v49, v44, v50
	v_mul_f32_e32 v51, 0x42800000, v60
	v_mul_f32_e32 v54, 0x42800000, v64
	v_mul_f32_e32 v44, 0x42800000, v56
	v_mul_f32_e32 v50, 0x42800000, v108
	v_cvt_pk_fp8_f32 v48, v51, v54 op_sel:[0,0,1]
	v_cvt_pk_fp8_f32 v49, v44, v50 op_sel:[0,0,1]
	v_mul_f32_e32 v50, 0x42800000, v69
	v_mul_f32_e32 v51, 0x42800000, v73
	v_mov_b32_e32 v44, v131
	v_cvt_pk_fp8_f32 v44, v50, v51
	v_mul_f32_e32 v50, 0x42800000, v45
	v_mul_f32_e32 v51, 0x42800000, v53
	v_mov_b32_e32 v45, v131
	v_cvt_pk_fp8_f32 v45, v50, v51
	v_mul_f32_e32 v52, 0x42800000, v61
	v_mul_f32_e32 v54, 0x42800000, v65
	v_mul_f32_e32 v50, 0x42800000, v57
	v_mul_f32_e32 v51, 0x42800000, v109
	v_cvt_pk_fp8_f32 v44, v52, v54 op_sel:[0,0,1]
	v_cvt_pk_fp8_f32 v45, v50, v51 op_sel:[0,0,1]
	ds_write_b64 v242, v[46:47]
	ds_write_b64 v242, v[42:43] offset:128
	ds_write_b64 v242, v[48:49] offset:256
	ds_write_b64 v242, v[44:45] offset:384
	ds_read_b128 v[42:45], v244
	v_cndmask_b32_e64 v46, v201, v200, s[6:7]
	v_or_b32_e32 v46, s8, v46
	v_mov_b32_e32 v47, v131
	v_lshlrev_b64 v[46:47], 11, v[46:47]
	v_lshl_add_u64 v[50:51], v[134:135], 0, v[46:47]
	ds_read_b128 v[46:49], v246
	s_waitcnt lgkmcnt(1)
	global_store_dwordx4 v[50:51], v[42:45], off
	s_waitcnt vmcnt(1)
	v_mul_f32_e32 v107, 0x42800000, v114
	v_mul_f32_e32 v108, 0x42800000, v110
	v_or_b32_e32 v42, 8, v200
	v_cndmask_b32_e64 v42, v202, v42, s[6:7]
	v_or_b32_e32 v42, s8, v42
	v_mov_b32_e32 v43, v131
	v_lshlrev_b64 v[42:43], 11, v[42:43]
	v_lshl_add_u64 v[42:43], v[134:135], 0, v[42:43]
	s_waitcnt lgkmcnt(0)
	global_store_dwordx4 v[42:43], v[46:49], off
	ds_read_b128 v[42:45], v248
	v_mov_b32_e32 v106, v131
	v_or_b32_e32 v46, 16, v200
	v_cndmask_b32_e64 v46, v210, v46, s[6:7]
	v_or_b32_e32 v46, s8, v46
	v_mov_b32_e32 v47, v131
	v_lshlrev_b64 v[46:47], 11, v[46:47]
	v_lshl_add_u64 v[50:51], v[134:135], 0, v[46:47]
	ds_read_b128 v[46:49], v250
	s_waitcnt lgkmcnt(1)
	global_store_dwordx4 v[50:51], v[42:45], off
	v_cvt_pk_fp8_f32 v106, v107, v108
	v_mul_f32_e32 v102, 0x42800000, v102
	v_cndmask_b32_e64 v42, v211, v203, s[6:7]
	v_or_b32_e32 v42, s8, v42
	v_mov_b32_e32 v43, v131
	v_lshlrev_b64 v[42:43], 11, v[42:43]
	v_lshl_add_u64 v[42:43], v[134:135], 0, v[42:43]
	s_waitcnt lgkmcnt(0)
	global_store_dwordx4 v[42:43], v[46:49], off
	ds_read_b128 v[42:45], v252
	v_mul_f32_e32 v98, 0x42800000, v98
	v_or_b32_e32 v46, 32, v200
	v_cndmask_b32_e64 v46, v212, v46, s[6:7]
	v_or_b32_e32 v46, s8, v46
	v_mov_b32_e32 v47, v131
	v_lshlrev_b64 v[46:47], 11, v[46:47]
	v_lshl_add_u64 v[50:51], v[134:135], 0, v[46:47]
	ds_read_b128 v[46:49], v204
	s_waitcnt lgkmcnt(1)
	global_store_dwordx4 v[50:51], v[42:45], off
	v_mov_b32_e32 v107, v131
	v_cvt_pk_fp8_f32 v107, v102, v98
	v_cndmask_b32_e64 v42, v213, v205, s[6:7]
	v_or_b32_e32 v42, s8, v42
	v_mov_b32_e32 v43, v131
	v_lshlrev_b64 v[42:43], 11, v[42:43]
	v_lshl_add_u64 v[42:43], v[134:135], 0, v[42:43]
	s_waitcnt lgkmcnt(0)
	global_store_dwordx4 v[42:43], v[46:49], off
	ds_read_b128 v[42:45], v216
	v_mul_f32_e32 v109, 0x42800000, v115
	v_cndmask_b32_e64 v46, v214, v228, s[6:7]
	v_or_b32_e32 v46, s8, v46
	v_mov_b32_e32 v47, v131
	v_lshlrev_b64 v[46:47], 11, v[46:47]
	v_lshl_add_u64 v[50:51], v[134:135], 0, v[46:47]
	ds_read_b128 v[46:49], v220
	s_waitcnt lgkmcnt(1)
	global_store_dwordx4 v[50:51], v[42:45], off
	v_mul_f32_e32 v110, 0x42800000, v111
	v_mul_f32_e32 v38, 0x42800000, v38
	v_cndmask_b32_e64 v42, v215, v232, s[6:7]
	v_or_b32_e32 v42, s8, v42
	v_mov_b32_e32 v43, v131
	v_lshlrev_b64 v[42:43], 11, v[42:43]
	v_lshl_add_u64 v[42:43], v[134:135], 0, v[42:43]
	s_waitcnt lgkmcnt(0)
	global_store_dwordx4 v[42:43], v[46:49], off
	global_load_dwordx4 v[74:77], v[136:137], off offset:256
	global_load_dwordx4 v[78:81], v[138:139], off offset:256
	global_load_dwordx4 v[94:97], v[140:141], off offset:256
	global_load_dwordx4 v[82:85], v[142:143], off offset:256
	global_load_dwordx4 v[70:73], v[144:145], off offset:256
	global_load_dwordx4 v[66:69], v[146:147], off offset:256
	global_load_dwordx4 v[58:61], v[148:149], off offset:256
	global_load_dwordx4 v[62:65], v[150:151], off offset:256
	global_load_dwordx4 v[42:45], v[152:153], off offset:256
	global_load_dwordx4 v[46:49], v[154:155], off offset:256
	v_mul_f32_e32 v34, 0x42800000, v34
	v_mov_b32_e32 v108, v131
	v_cvt_pk_fp8_f32 v107, v38, v34 op_sel:[0,0,1]
	v_cvt_pk_fp8_f32 v108, v109, v110
	v_mul_f32_e32 v34, 0x42800000, v103
	v_mul_f32_e32 v38, 0x42800000, v99
	v_mov_b32_e32 v109, v131
	v_cvt_pk_fp8_f32 v109, v34, v38
	v_mul_f32_e32 v34, 0x42800000, v91
	v_mul_f32_e32 v38, 0x42800000, v87
	v_cvt_pk_fp8_f32 v108, v34, v38 op_sel:[0,0,1]
	v_mul_f32_e32 v34, 0x42800000, v39
	v_mul_f32_e32 v35, 0x42800000, v35
	v_mul_f32_e32 v111, 0x42800000, v116
	v_mul_f32_e32 v112, 0x42800000, v112
	v_mul_f32_e32 v90, 0x42800000, v90
	v_mul_f32_e32 v86, 0x42800000, v86
	v_cvt_pk_fp8_f32 v109, v34, v35 op_sel:[0,0,1]
	v_mov_b32_e32 v34, v131
	v_cvt_pk_fp8_f32 v106, v90, v86 op_sel:[0,0,1]
	v_cvt_pk_fp8_f32 v34, v111, v112
	v_mul_f32_e32 v86, 0x42800000, v104
	v_mul_f32_e32 v87, 0x42800000, v100
	v_mov_b32_e32 v35, v131
	global_load_dwordx4 v[50:53], v[156:157], off offset:256
	global_load_dwordx4 v[54:57], v[158:159], off offset:256
	v_mul_f32_e32 v38, 0x42800000, v92
	v_mul_f32_e32 v110, 0x42800000, v93
	v_mul_f32_e32 v39, 0x42800000, v88
	v_mul_f32_e32 v115, 0x42800000, v89
	v_cvt_pk_fp8_f32 v35, v86, v87
	global_load_dwordx4 v[86:89], v[164:165], off offset:256
	global_load_dwordx4 v[90:93], v[166:167], off offset:256
	v_mul_f32_e32 v98, 0x42800000, v105
	v_mul_f32_e32 v99, 0x42800000, v101
	v_cvt_pk_fp8_f32 v34, v38, v39 op_sel:[0,0,1]
	v_mov_b32_e32 v39, v131
	v_cvt_pk_fp8_f32 v39, v98, v99
	global_load_dwordx4 v[98:101], v[160:161], off offset:256
	global_load_dwordx4 v[102:105], v[162:163], off offset:256
	v_mul_f32_e32 v38, 0x42800000, v40
	v_mul_f32_e32 v36, 0x42800000, v36
	v_mul_f32_e32 v114, 0x42800000, v117
	v_mul_f32_e32 v113, 0x42800000, v113
	v_cvt_pk_fp8_f32 v35, v38, v36 op_sel:[0,0,1]
	v_mov_b32_e32 v38, v131
	v_cvt_pk_fp8_f32 v38, v114, v113
	v_mul_f32_e32 v36, 0x42800000, v41
	v_mul_f32_e32 v37, 0x42800000, v37
	v_cvt_pk_fp8_f32 v39, v36, v37 op_sel:[0,0,1]
	v_cvt_pk_fp8_f32 v38, v110, v115 op_sel:[0,0,1]
	ds_write_b64 v236, v[106:107]
	ds_write_b64 v236, v[108:109] offset:128
	ds_write_b64 v236, v[34:35] offset:256
	ds_write_b64 v236, v[38:39] offset:384
	v_mul_f32_e32 v14, 0x42800000, v14
	v_mul_f32_e32 v10, 0x42800000, v10
	v_mov_b32_e32 v35, v131
	v_cvt_pk_fp8_f32 v35, v14, v10
	v_mul_f32_e32 v6, 0x42800000, v6
	v_mul_f32_e32 v2, 0x42800000, v2
	v_mov_b32_e32 v10, v131
	v_cvt_pk_fp8_f32 v35, v6, v2 op_sel:[0,0,1]
	v_mul_f32_e32 v2, 0x42800000, v31
	v_mul_f32_e32 v6, 0x42800000, v27
	v_cvt_pk_fp8_f32 v10, v2, v6
	v_mul_f32_e32 v2, 0x42800000, v15
	v_mul_f32_e32 v6, 0x42800000, v11
	v_mov_b32_e32 v11, v131
	v_cvt_pk_fp8_f32 v11, v2, v6
	v_mov_b32_e32 v106, v131
	v_mul_f32_e32 v30, 0x42800000, v30
	v_mul_f32_e32 v26, 0x42800000, v26
	v_mov_b32_e32 v34, v131
	v_mul_f32_e32 v2, 0x42800000, v7
	v_mul_f32_e32 v3, 0x42800000, v3
	s_waitcnt vmcnt(15)
	v_mul_f32_e32 v107, 0x42800000, v74
	s_waitcnt vmcnt(14)
	v_mul_f32_e32 v108, 0x42800000, v78
	v_cvt_pk_fp8_f32 v106, v107, v108
	v_mov_b32_e32 v107, v131
	s_waitcnt vmcnt(11)
	v_mul_f32_e32 v70, 0x42800000, v70
	s_waitcnt vmcnt(10)
	v_mul_f32_e32 v66, 0x42800000, v66
	v_cvt_pk_fp8_f32 v107, v70, v66
	v_cvt_pk_fp8_f32 v34, v30, v26
	v_cvt_pk_fp8_f32 v11, v2, v3 op_sel:[0,0,1]
	v_mul_f32_e32 v3, 0x42800000, v32
	v_mul_f32_e32 v6, 0x42800000, v28
	v_mov_b32_e32 v2, v131
	v_mul_f32_e32 v66, 0x42800000, v94
	v_mul_f32_e32 v70, 0x42800000, v82
	v_cvt_pk_fp8_f32 v2, v3, v6
	v_mul_f32_e32 v6, 0x42800000, v16
	v_mul_f32_e32 v12, 0x42800000, v12
	v_mov_b32_e32 v3, v131
	v_mul_f32_e32 v109, 0x42800000, v75
	v_mul_f32_e32 v110, 0x42800000, v79
	v_cvt_pk_fp8_f32 v106, v66, v70 op_sel:[0,0,1]
	s_waitcnt vmcnt(9)
	v_mul_f32_e32 v58, 0x42800000, v58
	s_waitcnt vmcnt(8)
	v_mul_f32_e32 v62, 0x42800000, v62
	v_mov_b32_e32 v66, v131
	v_cvt_pk_fp8_f32 v3, v6, v12
	v_cvt_pk_fp8_f32 v107, v58, v62 op_sel:[0,0,1]
	v_cvt_pk_fp8_f32 v66, v109, v110
	v_mul_f32_e32 v58, 0x42800000, v71
	v_mul_f32_e32 v62, 0x42800000, v67
	v_mov_b32_e32 v67, v131
	v_mul_f32_e32 v22, 0x42800000, v22
	v_mul_f32_e32 v18, 0x42800000, v18
	v_cvt_pk_fp8_f32 v67, v58, v62
	v_cvt_pk_fp8_f32 v34, v22, v18 op_sel:[0,0,1]
	v_mul_f32_e32 v14, 0x42800000, v23
	v_mul_f32_e32 v18, 0x42800000, v19
	v_cvt_pk_fp8_f32 v10, v14, v18 op_sel:[0,0,1]
	v_mul_f32_e32 v7, 0x42800000, v24
	v_mul_f32_e32 v14, 0x42800000, v20
	v_mul_f32_e32 v6, 0x42800000, v8
	v_mul_f32_e32 v4, 0x42800000, v4
	v_mul_f32_e32 v58, 0x42800000, v95
	v_mul_f32_e32 v62, 0x42800000, v83
	v_cvt_pk_fp8_f32 v2, v7, v14 op_sel:[0,0,1]
	v_cvt_pk_fp8_f32 v3, v6, v4 op_sel:[0,0,1]
	v_mul_f32_e32 v4, 0x42800000, v33
	v_mul_f32_e32 v7, 0x42800000, v29
	v_mov_b32_e32 v6, v131
	v_cvt_pk_fp8_f32 v66, v58, v62 op_sel:[0,0,1]
	v_mul_f32_e32 v58, 0x42800000, v59
	v_mul_f32_e32 v59, 0x42800000, v63
	v_cvt_pk_fp8_f32 v6, v4, v7
	v_mul_f32_e32 v4, 0x42800000, v17
	v_mul_f32_e32 v13, 0x42800000, v13
	v_mov_b32_e32 v7, v131
	v_mul_f32_e32 v111, 0x42800000, v76
	v_mul_f32_e32 v112, 0x42800000, v80
	v_cvt_pk_fp8_f32 v67, v58, v59 op_sel:[0,0,1]
	v_mov_b32_e32 v58, v131
	v_cvt_pk_fp8_f32 v7, v4, v13
	v_cvt_pk_fp8_f32 v58, v111, v112
	v_mul_f32_e32 v72, 0x42800000, v72
	v_mul_f32_e32 v68, 0x42800000, v68
	v_mov_b32_e32 v59, v131
	v_cvt_pk_fp8_f32 v59, v72, v68
	v_mul_f32_e32 v8, 0x42800000, v25
	v_mul_f32_e32 v12, 0x42800000, v21
	v_mul_f32_e32 v4, 0x42800000, v9
	v_mul_f32_e32 v5, 0x42800000, v5
	v_mul_f32_e32 v62, 0x42800000, v96
	v_mul_f32_e32 v63, 0x42800000, v84
	v_cvt_pk_fp8_f32 v6, v8, v12 op_sel:[0,0,1]
	v_cvt_pk_fp8_f32 v7, v4, v5 op_sel:[0,0,1]
	v_cvt_pk_fp8_f32 v58, v62, v63 op_sel:[0,0,1]
	v_mul_f32_e32 v60, 0x42800000, v60
	v_mul_f32_e32 v62, 0x42800000, v64
	ds_write_b64 v238, v[34:35]
	ds_write_b64 v238, v[10:11] offset:128
	ds_write_b64 v238, v[2:3] offset:256
	ds_write_b64 v238, v[6:7] offset:384
	v_mul_f32_e32 v113, 0x42800000, v77
	v_mul_f32_e32 v114, 0x42800000, v81
	v_mul_f32_e32 v68, 0x42800000, v73
	v_mul_f32_e32 v69, 0x42800000, v69
	v_cvt_pk_fp8_f32 v59, v60, v62 op_sel:[0,0,1]
	v_mov_b32_e32 v62, v131
	v_mov_b32_e32 v63, v131
	global_load_dwordx4 v[2:5], v[168:169], off offset:512
	global_load_dwordx4 v[6:9], v[170:171], off offset:512
	global_load_dwordx4 v[10:13], v[172:173], off offset:512
	global_load_dwordx4 v[14:17], v[174:175], off offset:512
	global_load_dwordx4 v[18:21], v[176:177], off offset:512
	global_load_dwordx4 v[22:25], v[178:179], off offset:512
	global_load_dwordx4 v[26:29], v[180:181], off offset:512
	global_load_dwordx4 v[30:33], v[182:183], off offset:512
	global_load_dwordx4 v[34:37], v[184:185], off offset:512
	global_load_dwordx4 v[38:41], v[186:187], off offset:512
	global_load_dwordx4 v[74:77], v[188:189], off offset:512
	global_load_dwordx4 v[78:81], v[190:191], off offset:512
	v_mul_f32_e32 v71, 0x42800000, v85
	global_load_dwordx4 v[122:125], v[192:193], off offset:512
	global_load_dwordx4 v[126:129], v[194:195], off offset:512
	v_cvt_pk_fp8_f32 v62, v113, v114
	v_cvt_pk_fp8_f32 v63, v68, v69
	global_load_dwordx4 v[82:85], v[196:197], off offset:512
	global_load_dwordx4 v[206:209], v[198:199], off offset:512
	v_mul_f32_e32 v70, 0x42800000, v97
	v_mul_f32_e32 v60, 0x42800000, v61
	v_mul_f32_e32 v61, 0x42800000, v65
	v_cvt_pk_fp8_f32 v62, v70, v71 op_sel:[0,0,1]
	v_cvt_pk_fp8_f32 v63, v60, v61 op_sel:[0,0,1]
	ds_write_b64 v240, v[106:107]
	ds_write_b64 v240, v[66:67] offset:128
	ds_write_b64 v240, v[58:59] offset:256
	ds_write_b64 v240, v[62:63] offset:384
	s_waitcnt vmcnt(23)
	v_mul_f32_e32 v42, 0x42800000, v42
	s_waitcnt vmcnt(22)
	v_mul_f32_e32 v46, 0x42800000, v46
	v_mov_b32_e32 v58, v131
	v_cvt_pk_fp8_f32 v58, v42, v46
	s_waitcnt vmcnt(19)
	v_mul_f32_e32 v42, 0x42800000, v86
	s_waitcnt vmcnt(18)
	v_mul_f32_e32 v46, 0x42800000, v90
	v_mov_b32_e32 v59, v131
	v_cvt_pk_fp8_f32 v59, v42, v46
	s_waitcnt vmcnt(17)
	v_mul_f32_e32 v42, 0x42800000, v98
	s_waitcnt vmcnt(16)
	v_mul_f32_e32 v46, 0x42800000, v102
	v_mul_f32_e32 v43, 0x42800000, v43
	v_cvt_pk_fp8_f32 v59, v42, v46 op_sel:[0,0,1]
	v_mul_f32_e32 v46, 0x42800000, v47
	v_mov_b32_e32 v42, v131
	v_mul_f32_e32 v47, 0x42800000, v51
	v_cvt_pk_fp8_f32 v42, v43, v46
	v_mul_f32_e32 v46, 0x42800000, v87
	v_mul_f32_e32 v51, 0x42800000, v91
	v_mov_b32_e32 v43, v131
	v_cvt_pk_fp8_f32 v43, v46, v51
	v_mul_f32_e32 v50, 0x42800000, v50
	v_mul_f32_e32 v54, 0x42800000, v54
	v_cvt_pk_fp8_f32 v58, v50, v54 op_sel:[0,0,1]
	v_mul_f32_e32 v50, 0x42800000, v55
	v_cvt_pk_fp8_f32 v42, v47, v50 op_sel:[0,0,1]
	v_mul_f32_e32 v46, 0x42800000, v99
	v_mul_f32_e32 v47, 0x42800000, v103
	v_cvt_pk_fp8_f32 v43, v46, v47 op_sel:[0,0,1]
	v_mul_f32_e32 v44, 0x42800000, v44
	v_mul_f32_e32 v47, 0x42800000, v48
	v_mov_b32_e32 v46, v131
	v_cvt_pk_fp8_f32 v46, v44, v47
	v_mul_f32_e32 v44, 0x42800000, v88
	v_mul_f32_e32 v51, 0x42800000, v92
	v_mov_b32_e32 v47, v131
	v_cvt_pk_fp8_f32 v47, v44, v51
	v_mul_f32_e32 v48, 0x42800000, v52
	v_mul_f32_e32 v50, 0x42800000, v56
	v_cvt_pk_fp8_f32 v46, v48, v50 op_sel:[0,0,1]
	v_mul_f32_e32 v44, 0x42800000, v100
	v_mul_f32_e32 v48, 0x42800000, v104
	v_cvt_pk_fp8_f32 v47, v44, v48 op_sel:[0,0,1]
	v_mul_f32_e32 v45, 0x42800000, v45
	v_mul_f32_e32 v48, 0x42800000, v49
	v_mov_b32_e32 v44, v131
	v_cvt_pk_fp8_f32 v44, v45, v48
	v_mul_f32_e32 v48, 0x42800000, v89
	v_mul_f32_e32 v51, 0x42800000, v93
	v_mov_b32_e32 v45, v131
	v_cvt_pk_fp8_f32 v45, v48, v51
	v_mul_f32_e32 v49, 0x42800000, v53
	v_mul_f32_e32 v50, 0x42800000, v57
	v_cvt_pk_fp8_f32 v44, v49, v50 op_sel:[0,0,1]
	v_mul_f32_e32 v48, 0x42800000, v101
	v_mul_f32_e32 v49, 0x42800000, v105
	v_cvt_pk_fp8_f32 v45, v48, v49 op_sel:[0,0,1]
	ds_write_b64 v242, v[58:59]
	ds_write_b64 v242, v[42:43] offset:128
	ds_write_b64 v242, v[46:47] offset:256
	ds_write_b64 v242, v[44:45] offset:384
	ds_read_b128 v[42:45], v244
	v_or_b32_e32 v46, 64, v200
	v_cndmask_b32_e64 v46, v217, v46, s[6:7]
	v_or_b32_e32 v46, s8, v46
	v_mov_b32_e32 v47, v131
	v_lshlrev_b64 v[46:47], 11, v[46:47]
	v_lshl_add_u64 v[50:51], v[134:135], 0, v[46:47]
	ds_read_b128 v[46:49], v246
	s_waitcnt lgkmcnt(1)
	global_store_dwordx4 v[50:51], v[42:45], off
	s_waitcnt vmcnt(8)
	v_mul_f32_e32 v34, 0x42800000, v34
	s_waitcnt vmcnt(7)
	v_mul_f32_e32 v38, 0x42800000, v38
	v_or_b32_e32 v42, 0x48, v200
	v_cndmask_b32_e64 v42, v219, v42, s[6:7]
	v_or_b32_e32 v42, s8, v42
	v_mov_b32_e32 v43, v131
	v_lshlrev_b64 v[42:43], 11, v[42:43]
	v_lshl_add_u64 v[42:43], v[134:135], 0, v[42:43]
	s_waitcnt lgkmcnt(0)
	global_store_dwordx4 v[42:43], v[46:49], off
	ds_read_b128 v[42:45], v248
	v_mul_f32_e32 v35, 0x42800000, v35
	v_or_b32_e32 v46, 0x50, v200
	v_cndmask_b32_e64 v46, v221, v46, s[6:7]
	v_or_b32_e32 v46, s8, v46
	v_mov_b32_e32 v47, v131
	v_lshlrev_b64 v[46:47], 11, v[46:47]
	v_lshl_add_u64 v[50:51], v[134:135], 0, v[46:47]
	ds_read_b128 v[46:49], v250
	s_waitcnt lgkmcnt(1)
	global_store_dwordx4 v[50:51], v[42:45], off
	v_mul_f32_e32 v36, 0x42800000, v36
	v_mul_f32_e32 v37, 0x42800000, v37
	v_or_b32_e32 v42, 0x58, v200
	v_cndmask_b32_e64 v42, v223, v42, s[6:7]
	v_or_b32_e32 v42, s8, v42
	v_mov_b32_e32 v43, v131
	v_lshlrev_b64 v[42:43], 11, v[42:43]
	v_lshl_add_u64 v[42:43], v[134:135], 0, v[42:43]
	s_waitcnt lgkmcnt(0)
	global_store_dwordx4 v[42:43], v[46:49], off
	ds_read_b128 v[42:45], v252
	v_mul_f32_e32 v14, 0x42800000, v14
	v_or_b32_e32 v46, 0x60, v200
	v_cndmask_b32_e64 v46, v225, v46, s[6:7]
	v_or_b32_e32 v46, s8, v46
	v_mov_b32_e32 v47, v131
	v_lshlrev_b64 v[46:47], 11, v[46:47]
	v_lshl_add_u64 v[50:51], v[134:135], 0, v[46:47]
	ds_read_b128 v[46:49], v204
	s_waitcnt lgkmcnt(1)
	global_store_dwordx4 v[50:51], v[42:45], off
	v_mul_f32_e32 v10, 0x42800000, v10
	v_mul_f32_e32 v6, 0x42800000, v6
	v_or_b32_e32 v42, 0x68, v200
	v_cndmask_b32_e64 v42, v227, v42, s[6:7]
	v_or_b32_e32 v42, s8, v42
	v_mov_b32_e32 v43, v131
	v_lshlrev_b64 v[42:43], 11, v[42:43]
	v_lshl_add_u64 v[42:43], v[134:135], 0, v[42:43]
	s_waitcnt lgkmcnt(0)
	global_store_dwordx4 v[42:43], v[46:49], off
	ds_read_b128 v[42:45], v216
	v_mul_f32_e32 v2, 0x42800000, v2
	v_or_b32_e32 v46, 0x70, v200
	v_cndmask_b32_e64 v46, v229, v46, s[6:7]
	v_or_b32_e32 v46, s8, v46
	v_mov_b32_e32 v47, v131
	v_lshlrev_b64 v[46:47], 11, v[46:47]
	v_lshl_add_u64 v[50:51], v[134:135], 0, v[46:47]
	ds_read_b128 v[46:49], v220
	s_waitcnt lgkmcnt(1)
	global_store_dwordx4 v[50:51], v[42:45], off
	s_waitcnt vmcnt(12)
	v_mul_f32_e32 v51, 0x42800000, v74
	s_waitcnt vmcnt(8)
	v_mul_f32_e32 v50, 0x42800000, v85
	v_or_b32_e32 v42, 0x78, v200
	v_cndmask_b32_e64 v42, v231, v42, s[6:7]
	v_or_b32_e32 v42, s8, v42
	v_mov_b32_e32 v43, v131
	v_lshlrev_b64 v[42:43], 11, v[42:43]
	v_lshl_add_u64 v[42:43], v[134:135], 0, v[42:43]
	s_waitcnt lgkmcnt(0)
	global_store_dwordx4 v[42:43], v[46:49], off
	global_load_dwordx4 v[106:109], v[136:137], off offset:512
	global_load_dwordx4 v[110:113], v[138:139], off offset:512
	global_load_dwordx4 v[114:117], v[140:141], off offset:512
	global_load_dwordx4 v[118:121], v[142:143], off offset:512
	global_load_dwordx4 v[98:101], v[144:145], off offset:512
	global_load_dwordx4 v[102:105], v[146:147], off offset:512
	global_load_dwordx4 v[90:93], v[148:149], off offset:512
	global_load_dwordx4 v[94:97], v[150:151], off offset:512
	global_load_dwordx4 v[66:69], v[152:153], off offset:512
	global_load_dwordx4 v[70:73], v[154:155], off offset:512
	s_waitcnt vmcnt(18)
	v_mul_f32_e32 v43, 0x42800000, v206
	v_mul_f32_e32 v44, 0x42800000, v82
	v_mov_b32_e32 v42, v131
	v_cvt_pk_fp8_f32 v42, v43, v44
	v_mul_f32_e32 v44, 0x42800000, v78
	v_mov_b32_e32 v43, v131
	v_cvt_pk_fp8_f32 v43, v44, v51
	v_mul_f32_e32 v44, 0x42800000, v126
	v_mul_f32_e32 v51, 0x42800000, v122
	v_mul_f32_e32 v45, 0x42800000, v207
	v_mul_f32_e32 v46, 0x42800000, v83
	v_cvt_pk_fp8_f32 v42, v44, v51 op_sel:[0,0,1]
	v_mov_b32_e32 v44, v131
	v_cvt_pk_fp8_f32 v43, v38, v34 op_sel:[0,0,1]
	v_cvt_pk_fp8_f32 v44, v45, v46
	v_mul_f32_e32 v34, 0x42800000, v79
	v_mul_f32_e32 v38, 0x42800000, v75
	v_mov_b32_e32 v45, v131
	v_cvt_pk_fp8_f32 v45, v34, v38
	v_mul_f32_e32 v34, 0x42800000, v127
	v_mul_f32_e32 v38, 0x42800000, v123
	v_cvt_pk_fp8_f32 v44, v34, v38 op_sel:[0,0,1]
	v_mul_f32_e32 v34, 0x42800000, v39
	v_mul_f32_e32 v47, 0x42800000, v208
	v_mul_f32_e32 v48, 0x42800000, v84
	v_cvt_pk_fp8_f32 v45, v34, v35 op_sel:[0,0,1]
	v_mov_b32_e32 v34, v131
	v_cvt_pk_fp8_f32 v34, v47, v48
	v_mul_f32_e32 v47, 0x42800000, v80
	v_mul_f32_e32 v48, 0x42800000, v76
	v_mov_b32_e32 v35, v131
	global_load_dwordx4 v[82:85], v[156:157], off offset:512
	global_load_dwordx4 v[86:89], v[158:159], off offset:512
	v_mul_f32_e32 v39, 0x42800000, v124
	v_mul_f32_e32 v51, 0x42800000, v125
	v_cvt_pk_fp8_f32 v35, v47, v48
	v_mul_f32_e32 v47, 0x42800000, v81
	global_load_dwordx4 v[78:81], v[164:165], off offset:512
	global_load_dwordx4 v[122:125], v[166:167], off offset:512
	v_mul_f32_e32 v38, 0x42800000, v128
	v_mul_f32_e32 v46, 0x42800000, v129
	v_mul_f32_e32 v48, 0x42800000, v77
	global_load_dwordx4 v[74:77], v[160:161], off offset:512
	global_load_dwordx4 v[126:129], v[162:163], off offset:512
	v_cvt_pk_fp8_f32 v34, v38, v39 op_sel:[0,0,1]
	v_mul_f32_e32 v38, 0x42800000, v40
	v_mul_f32_e32 v49, 0x42800000, v209
	v_cvt_pk_fp8_f32 v35, v38, v36 op_sel:[0,0,1]
	v_mov_b32_e32 v38, v131
	v_mov_b32_e32 v39, v131
	v_cvt_pk_fp8_f32 v38, v49, v50
	v_cvt_pk_fp8_f32 v39, v47, v48
	v_mul_f32_e32 v36, 0x42800000, v41
	v_mul_f32_e32 v30, 0x42800000, v30
	v_cvt_pk_fp8_f32 v38, v46, v51 op_sel:[0,0,1]
	v_cvt_pk_fp8_f32 v39, v36, v37 op_sel:[0,0,1]
	ds_write_b64 v236, v[42:43]
	ds_write_b64 v236, v[44:45] offset:128
	ds_write_b64 v236, v[34:35] offset:256
	ds_write_b64 v236, v[38:39] offset:384
	v_mov_b32_e32 v35, v131
	v_cvt_pk_fp8_f32 v35, v14, v10
	v_mov_b32_e32 v10, v131
	v_mul_f32_e32 v26, 0x42800000, v26
	v_mov_b32_e32 v34, v131
	v_cvt_pk_fp8_f32 v35, v6, v2 op_sel:[0,0,1]
	v_mul_f32_e32 v2, 0x42800000, v31
	v_mul_f32_e32 v6, 0x42800000, v27
	v_cvt_pk_fp8_f32 v10, v2, v6
	v_mul_f32_e32 v2, 0x42800000, v15
	v_mul_f32_e32 v6, 0x42800000, v11
	v_mov_b32_e32 v11, v131
	v_cvt_pk_fp8_f32 v11, v2, v6
	v_mul_f32_e32 v2, 0x42800000, v7
	v_mul_f32_e32 v3, 0x42800000, v3
	v_cvt_pk_fp8_f32 v34, v30, v26
	v_cvt_pk_fp8_f32 v11, v2, v3 op_sel:[0,0,1]
	v_mul_f32_e32 v3, 0x42800000, v32
	v_mul_f32_e32 v6, 0x42800000, v28
	v_mov_b32_e32 v2, v131
	v_cvt_pk_fp8_f32 v2, v3, v6
	v_mul_f32_e32 v6, 0x42800000, v16
	v_mul_f32_e32 v12, 0x42800000, v12
	v_mov_b32_e32 v3, v131
	v_cvt_pk_fp8_f32 v3, v6, v12
	v_mul_f32_e32 v22, 0x42800000, v22
	v_mul_f32_e32 v18, 0x42800000, v18
	v_cvt_pk_fp8_f32 v34, v22, v18 op_sel:[0,0,1]
	v_mul_f32_e32 v14, 0x42800000, v23
	v_mul_f32_e32 v18, 0x42800000, v19
	v_cvt_pk_fp8_f32 v10, v14, v18 op_sel:[0,0,1]
	v_mul_f32_e32 v7, 0x42800000, v24
	v_mul_f32_e32 v14, 0x42800000, v20
	v_mul_f32_e32 v6, 0x42800000, v8
	v_mul_f32_e32 v4, 0x42800000, v4
	v_cvt_pk_fp8_f32 v2, v7, v14 op_sel:[0,0,1]
	v_cvt_pk_fp8_f32 v3, v6, v4 op_sel:[0,0,1]
	v_mul_f32_e32 v4, 0x42800000, v33
	v_mul_f32_e32 v7, 0x42800000, v29
	v_mov_b32_e32 v6, v131
	v_cvt_pk_fp8_f32 v6, v4, v7
	v_mul_f32_e32 v4, 0x42800000, v17
	v_mul_f32_e32 v13, 0x42800000, v13
	v_mov_b32_e32 v7, v131
	v_cvt_pk_fp8_f32 v7, v4, v13
	v_mul_f32_e32 v8, 0x42800000, v25
	v_mul_f32_e32 v12, 0x42800000, v21
	v_mul_f32_e32 v4, 0x42800000, v9
	v_mul_f32_e32 v5, 0x42800000, v5
	v_cvt_pk_fp8_f32 v6, v8, v12 op_sel:[0,0,1]
	v_cvt_pk_fp8_f32 v7, v4, v5 op_sel:[0,0,1]
	ds_write_b64 v238, v[34:35]
	ds_write_b64 v238, v[10:11] offset:128
	ds_write_b64 v238, v[2:3] offset:256
	ds_write_b64 v238, v[6:7] offset:384
	global_load_dwordx4 v[58:61], v[198:199], off offset:768
	global_load_dwordx4 v[62:65], v[196:197], off offset:768
	global_load_dwordx4 v[50:53], v[194:195], off offset:768
	global_load_dwordx4 v[42:45], v[192:193], off offset:768
	global_load_dwordx4 v[54:57], v[190:191], off offset:768
	global_load_dwordx4 v[34:37], v[188:189], off offset:768
	global_load_dwordx4 v[38:41], v[186:187], off offset:768
	global_load_dwordx4 v[46:49], v[184:185], off offset:768
	global_load_dwordx4 v[2:5], v[182:183], off offset:768
	global_load_dwordx4 v[6:9], v[180:181], off offset:768
	global_load_dwordx4 v[10:13], v[178:179], off offset:768
	global_load_dwordx4 v[14:17], v[176:177], off offset:768
	global_load_dwordx4 v[18:21], v[174:175], off offset:768
	global_load_dwordx4 v[22:25], v[172:173], off offset:768
	global_load_dwordx4 v[26:29], v[170:171], off offset:768
	global_load_dwordx4 v[30:33], v[168:169], off offset:768
	s_waitcnt vmcnt(27)
	v_mul_f32_e32 v98, 0x42800000, v98
	s_waitcnt vmcnt(26)
	v_mul_f32_e32 v102, 0x42800000, v102
	v_mov_b32_e32 v169, v131
	v_cvt_pk_fp8_f32 v169, v98, v102
	s_waitcnt vmcnt(25)
	v_mul_f32_e32 v90, 0x42800000, v90
	s_waitcnt vmcnt(24)
	v_mul_f32_e32 v94, 0x42800000, v94
	v_mov_b32_e32 v98, v131
	v_cvt_pk_fp8_f32 v169, v90, v94 op_sel:[0,0,1]
	v_mul_f32_e32 v90, 0x42800000, v107
	v_mul_f32_e32 v94, 0x42800000, v111
	v_cvt_pk_fp8_f32 v98, v90, v94
	v_mul_f32_e32 v90, 0x42800000, v99
	v_mul_f32_e32 v94, 0x42800000, v103
	v_mov_b32_e32 v99, v131
	v_cvt_pk_fp8_f32 v99, v90, v94
	v_mul_f32_e32 v90, 0x42800000, v91
	v_mul_f32_e32 v91, 0x42800000, v95
	v_mul_f32_e32 v94, 0x42800000, v112
	v_cvt_pk_fp8_f32 v99, v90, v91 op_sel:[0,0,1]
	v_mul_f32_e32 v91, 0x42800000, v108
	v_mov_b32_e32 v90, v131
	v_cvt_pk_fp8_f32 v90, v91, v94
	v_mul_f32_e32 v94, 0x42800000, v100
	v_mul_f32_e32 v100, 0x42800000, v104
	v_mov_b32_e32 v91, v131
	v_cvt_pk_fp8_f32 v91, v94, v100
	v_mul_f32_e32 v106, 0x42800000, v106
	v_mul_f32_e32 v110, 0x42800000, v110
	v_mov_b32_e32 v168, v131
	v_cvt_pk_fp8_f32 v168, v106, v110
	v_mul_f32_e32 v102, 0x42800000, v115
	v_mul_f32_e32 v106, 0x42800000, v119
	v_cvt_pk_fp8_f32 v98, v102, v106 op_sel:[0,0,1]
	v_mul_f32_e32 v95, 0x42800000, v116
	v_mul_f32_e32 v102, 0x42800000, v120
	v_mul_f32_e32 v92, 0x42800000, v92
	v_mul_f32_e32 v94, 0x42800000, v96
	v_cvt_pk_fp8_f32 v90, v95, v102 op_sel:[0,0,1]
	v_cvt_pk_fp8_f32 v91, v92, v94 op_sel:[0,0,1]
	v_mul_f32_e32 v92, 0x42800000, v109
	v_mul_f32_e32 v95, 0x42800000, v113
	v_mov_b32_e32 v94, v131
	v_cvt_pk_fp8_f32 v94, v92, v95
	v_mul_f32_e32 v92, 0x42800000, v101
	v_mul_f32_e32 v101, 0x42800000, v105
	v_mov_b32_e32 v95, v131
	v_mul_f32_e32 v114, 0x42800000, v114
	v_mul_f32_e32 v118, 0x42800000, v118
	v_cvt_pk_fp8_f32 v95, v92, v101
	v_cvt_pk_fp8_f32 v168, v114, v118 op_sel:[0,0,1]
	v_mul_f32_e32 v96, 0x42800000, v117
	v_mul_f32_e32 v100, 0x42800000, v121
	v_mul_f32_e32 v92, 0x42800000, v93
	v_mul_f32_e32 v93, 0x42800000, v97
	v_cvt_pk_fp8_f32 v94, v96, v100 op_sel:[0,0,1]
	v_cvt_pk_fp8_f32 v95, v92, v93 op_sel:[0,0,1]
	ds_write_b64 v240, v[168:169]
	ds_write_b64 v240, v[98:99] offset:128
	ds_write_b64 v240, v[90:91] offset:256
	ds_write_b64 v240, v[94:95] offset:384
	s_waitcnt vmcnt(23)
	v_mul_f32_e32 v66, 0x42800000, v66
	s_waitcnt vmcnt(22)
	v_mul_f32_e32 v70, 0x42800000, v70
	v_mov_b32_e32 v90, v131
	v_cvt_pk_fp8_f32 v90, v66, v70
	s_waitcnt vmcnt(19)
	v_mul_f32_e32 v66, 0x42800000, v78
	s_waitcnt vmcnt(18)
	v_mul_f32_e32 v70, 0x42800000, v122
	v_mov_b32_e32 v91, v131
	v_cvt_pk_fp8_f32 v91, v66, v70
	s_waitcnt vmcnt(17)
	v_mul_f32_e32 v66, 0x42800000, v74
	s_waitcnt vmcnt(16)
	v_mul_f32_e32 v70, 0x42800000, v126
	v_mul_f32_e32 v67, 0x42800000, v67
	v_cvt_pk_fp8_f32 v91, v66, v70 op_sel:[0,0,1]
	v_mul_f32_e32 v70, 0x42800000, v71
	v_mov_b32_e32 v66, v131
	v_cvt_pk_fp8_f32 v66, v67, v70
	v_mul_f32_e32 v70, 0x42800000, v79
	v_mul_f32_e32 v78, 0x42800000, v123
	v_mov_b32_e32 v67, v131
	v_cvt_pk_fp8_f32 v67, v70, v78
	v_mul_f32_e32 v71, 0x42800000, v83
	v_mul_f32_e32 v74, 0x42800000, v87
	v_cvt_pk_fp8_f32 v66, v71, v74 op_sel:[0,0,1]
	v_mul_f32_e32 v70, 0x42800000, v75
	v_mul_f32_e32 v71, 0x42800000, v127
	v_cvt_pk_fp8_f32 v67, v70, v71 op_sel:[0,0,1]
	v_mul_f32_e32 v68, 0x42800000, v68
	v_mul_f32_e32 v71, 0x42800000, v72
	v_mov_b32_e32 v70, v131
	v_cvt_pk_fp8_f32 v70, v68, v71
	v_mul_f32_e32 v68, 0x42800000, v80
	v_mul_f32_e32 v75, 0x42800000, v124
	v_mov_b32_e32 v71, v131
	v_cvt_pk_fp8_f32 v71, v68, v75
	v_mul_f32_e32 v72, 0x42800000, v84
	v_mul_f32_e32 v74, 0x42800000, v88
	v_cvt_pk_fp8_f32 v70, v72, v74 op_sel:[0,0,1]
	v_mul_f32_e32 v68, 0x42800000, v76
	v_mul_f32_e32 v72, 0x42800000, v128
	v_cvt_pk_fp8_f32 v71, v68, v72 op_sel:[0,0,1]
	v_mul_f32_e32 v69, 0x42800000, v69
	v_mul_f32_e32 v72, 0x42800000, v73
	v_mov_b32_e32 v68, v131
	v_cvt_pk_fp8_f32 v68, v69, v72
	v_mul_f32_e32 v72, 0x42800000, v81
	v_mul_f32_e32 v75, 0x42800000, v125
	v_mov_b32_e32 v69, v131
	v_mul_f32_e32 v82, 0x42800000, v82
	v_mul_f32_e32 v86, 0x42800000, v86
	v_cvt_pk_fp8_f32 v69, v72, v75
	v_cvt_pk_fp8_f32 v90, v82, v86 op_sel:[0,0,1]
	v_mul_f32_e32 v73, 0x42800000, v85
	v_mul_f32_e32 v74, 0x42800000, v89
	v_cvt_pk_fp8_f32 v68, v73, v74 op_sel:[0,0,1]
	v_mul_f32_e32 v72, 0x42800000, v77
	v_mul_f32_e32 v73, 0x42800000, v129
	v_cvt_pk_fp8_f32 v69, v72, v73 op_sel:[0,0,1]
	ds_write_b64 v242, v[90:91]
	ds_write_b64 v242, v[66:67] offset:128
	ds_write_b64 v242, v[70:71] offset:256
	ds_write_b64 v242, v[68:69] offset:384
	ds_read_b128 v[66:69], v244
	v_or_b32_e32 v70, 0x80, v200
	v_cndmask_b32_e64 v70, v233, v70, s[6:7]
	v_or_b32_e32 v70, s8, v70
	v_mov_b32_e32 v71, v131
	v_lshlrev_b64 v[70:71], 11, v[70:71]
	v_lshl_add_u64 v[74:75], v[134:135], 0, v[70:71]
	ds_read_b128 v[70:73], v246
	s_waitcnt lgkmcnt(1)
	global_store_dwordx4 v[74:75], v[66:69], off
	s_waitcnt vmcnt(16)
	v_mul_f32_e32 v90, 0x42800000, v58
	s_waitcnt vmcnt(15)
	v_mul_f32_e32 v91, 0x42800000, v62
	v_or_b32_e32 v66, 0x88, v200
	v_cndmask_b32_e64 v66, v235, v66, s[6:7]
	v_or_b32_e32 v66, s8, v66
	v_mov_b32_e32 v67, v131
	v_lshlrev_b64 v[66:67], 11, v[66:67]
	v_lshl_add_u64 v[66:67], v[134:135], 0, v[66:67]
	s_waitcnt lgkmcnt(0)
	global_store_dwordx4 v[66:67], v[70:73], off
	ds_read_b128 v[66:69], v248
	s_waitcnt vmcnt(15)
	v_mul_f32_e32 v92, 0x42800000, v50
	v_or_b32_e32 v70, 0x90, v200
	v_cndmask_b32_e64 v70, v237, v70, s[6:7]
	v_or_b32_e32 v70, s8, v70
	v_mov_b32_e32 v71, v131
	v_lshlrev_b64 v[70:71], 11, v[70:71]
	v_lshl_add_u64 v[74:75], v[134:135], 0, v[70:71]
	ds_read_b128 v[70:73], v250
	s_waitcnt lgkmcnt(1)
	global_store_dwordx4 v[74:75], v[66:69], off
	s_waitcnt vmcnt(15)
	v_mul_f32_e32 v93, 0x42800000, v42
	s_andn2_b64 vcc, exec, s[16:17]
	v_or_b32_e32 v66, 0x98, v200
	v_cndmask_b32_e64 v66, v239, v66, s[6:7]
	v_or_b32_e32 v66, s8, v66
	v_mov_b32_e32 v67, v131
	v_lshlrev_b64 v[66:67], 11, v[66:67]
	v_lshl_add_u64 v[66:67], v[134:135], 0, v[66:67]
	s_waitcnt lgkmcnt(0)
	global_store_dwordx4 v[66:67], v[70:73], off
	ds_read_b128 v[66:69], v252
	s_nop 0
	v_or_b32_e32 v70, 0xa0, v200
	v_cndmask_b32_e64 v70, v241, v70, s[6:7]
	v_or_b32_e32 v70, s8, v70
	v_mov_b32_e32 v71, v131
	v_lshlrev_b64 v[70:71], 11, v[70:71]
	v_lshl_add_u64 v[74:75], v[134:135], 0, v[70:71]
	ds_read_b128 v[70:73], v204
	s_waitcnt lgkmcnt(1)
	global_store_dwordx4 v[74:75], v[66:69], off
	s_nop 1
	v_or_b32_e32 v66, 0xa8, v200
	v_cndmask_b32_e64 v66, v243, v66, s[6:7]
	v_or_b32_e32 v66, s8, v66
	v_mov_b32_e32 v67, v131
	v_lshlrev_b64 v[66:67], 11, v[66:67]
	v_lshl_add_u64 v[66:67], v[134:135], 0, v[66:67]
	s_waitcnt lgkmcnt(0)
	global_store_dwordx4 v[66:67], v[70:73], off
	ds_read_b128 v[66:69], v216
	s_nop 0
	v_or_b32_e32 v70, 0xb0, v200
	v_cndmask_b32_e64 v70, v245, v70, s[6:7]
	v_or_b32_e32 v70, s8, v70
	v_mov_b32_e32 v71, v131
	v_lshlrev_b64 v[70:71], 11, v[70:71]
	v_lshl_add_u64 v[74:75], v[134:135], 0, v[70:71]
	ds_read_b128 v[70:73], v220
	s_waitcnt lgkmcnt(1)
	global_store_dwordx4 v[74:75], v[66:69], off
	s_nop 1
	v_or_b32_e32 v66, 0xb8, v200
	v_cndmask_b32_e64 v66, v247, v66, s[6:7]
	v_or_b32_e32 v66, s8, v66
	v_mov_b32_e32 v67, v131
	v_lshlrev_b64 v[66:67], 11, v[66:67]
	v_lshl_add_u64 v[66:67], v[134:135], 0, v[66:67]
	s_waitcnt lgkmcnt(0)
	global_store_dwordx4 v[66:67], v[70:73], off
	global_load_dwordx4 v[114:117], v[136:137], off offset:768
	global_load_dwordx4 v[118:121], v[138:139], off offset:768
	global_load_dwordx4 v[122:125], v[140:141], off offset:768
	global_load_dwordx4 v[126:129], v[142:143], off offset:768
	global_load_dwordx4 v[106:109], v[144:145], off offset:768
	global_load_dwordx4 v[110:113], v[146:147], off offset:768
	global_load_dwordx4 v[98:101], v[148:149], off offset:768
	global_load_dwordx4 v[102:105], v[150:151], off offset:768
	global_load_dwordx4 v[74:77], v[152:153], off offset:768
	global_load_dwordx4 v[78:81], v[154:155], off offset:768
	global_load_dwordx4 v[82:85], v[156:157], off offset:768
	global_load_dwordx4 v[86:89], v[158:159], off offset:768
	global_load_dwordx4 v[66:69], v[164:165], off offset:768
	global_load_dwordx4 v[70:73], v[166:167], off offset:768
	v_mov_b32_e32 v136, v131
	v_cvt_pk_fp8_f32 v136, v90, v91
	s_waitcnt vmcnt(33)
	v_mul_f32_e32 v90, 0x42800000, v54
	s_waitcnt vmcnt(32)
	v_mul_f32_e32 v91, 0x42800000, v34
	v_mov_b32_e32 v137, v131
	v_cvt_pk_fp8_f32 v137, v90, v91
	s_waitcnt vmcnt(31)
	v_mul_f32_e32 v90, 0x42800000, v38
	s_waitcnt vmcnt(30)
	v_mul_f32_e32 v91, 0x42800000, v46
	v_mov_b32_e32 v138, v131
	v_cvt_pk_fp8_f32 v137, v90, v91 op_sel:[0,0,1]
	v_mul_f32_e32 v90, 0x42800000, v59
	v_mul_f32_e32 v91, 0x42800000, v63
	v_cvt_pk_fp8_f32 v138, v90, v91
	v_mul_f32_e32 v90, 0x42800000, v55
	v_mul_f32_e32 v91, 0x42800000, v35
	v_mov_b32_e32 v139, v131
	v_cvt_pk_fp8_f32 v139, v90, v91
	v_mul_f32_e32 v90, 0x42800000, v39
	v_mul_f32_e32 v91, 0x42800000, v47
	v_mov_b32_e32 v140, v131
	v_cvt_pk_fp8_f32 v139, v90, v91 op_sel:[0,0,1]
	v_mul_f32_e32 v90, 0x42800000, v60
	v_mul_f32_e32 v91, 0x42800000, v64
	v_cvt_pk_fp8_f32 v140, v90, v91
	v_mul_f32_e32 v90, 0x42800000, v56
	v_mul_f32_e32 v91, 0x42800000, v36
	v_mov_b32_e32 v141, v131
	v_cvt_pk_fp8_f32 v141, v90, v91
	v_cvt_pk_fp8_f32 v136, v92, v93 op_sel:[0,0,1]
	v_mul_f32_e32 v92, 0x42800000, v51
	v_mul_f32_e32 v93, 0x42800000, v43
	v_cvt_pk_fp8_f32 v138, v92, v93 op_sel:[0,0,1]
	v_mul_f32_e32 v92, 0x42800000, v52
	v_mul_f32_e32 v93, 0x42800000, v44
	v_mul_f32_e32 v90, 0x42800000, v40
	v_mul_f32_e32 v91, 0x42800000, v48
	v_cvt_pk_fp8_f32 v140, v92, v93 op_sel:[0,0,1]
	v_cvt_pk_fp8_f32 v141, v90, v91 op_sel:[0,0,1]
	global_load_dwordx4 v[90:93], v[160:161], off offset:768
	global_load_dwordx4 v[94:97], v[162:163], off offset:768
	ds_write_b64 v236, v[136:137]
	ds_write_b64 v236, v[138:139] offset:128
	ds_write_b64 v236, v[140:141] offset:256
	v_mul_f32_e32 v137, 0x42800000, v61
	v_mul_f32_e32 v138, 0x42800000, v65
	v_mov_b32_e32 v136, v131
	v_cvt_pk_fp8_f32 v136, v137, v138
	v_mul_f32_e32 v138, 0x42800000, v57
	v_mul_f32_e32 v141, 0x42800000, v37
	v_mov_b32_e32 v137, v131
	v_cvt_pk_fp8_f32 v137, v138, v141
	v_mul_f32_e32 v139, 0x42800000, v53
	v_mul_f32_e32 v140, 0x42800000, v45
	v_cvt_pk_fp8_f32 v136, v139, v140 op_sel:[0,0,1]
	v_mul_f32_e32 v138, 0x42800000, v41
	v_mul_f32_e32 v139, 0x42800000, v49
	v_cvt_pk_fp8_f32 v137, v138, v139 op_sel:[0,0,1]
	s_waitcnt vmcnt(31)
	v_mul_f32_e32 v139, 0x42800000, v2
	s_waitcnt vmcnt(30)
	v_mul_f32_e32 v140, 0x42800000, v6
	v_mov_b32_e32 v138, v131
	v_cvt_pk_fp8_f32 v138, v139, v140
	s_waitcnt vmcnt(27)
	v_mul_f32_e32 v140, 0x42800000, v18
	s_waitcnt vmcnt(26)
	v_mul_f32_e32 v143, 0x42800000, v22
	v_mov_b32_e32 v139, v131
	v_cvt_pk_fp8_f32 v139, v140, v143
	v_mul_f32_e32 v141, 0x42800000, v10
	v_mul_f32_e32 v142, 0x42800000, v14
	v_cvt_pk_fp8_f32 v138, v141, v142 op_sel:[0,0,1]
	s_waitcnt vmcnt(25)
	v_mul_f32_e32 v140, 0x42800000, v26
	s_waitcnt vmcnt(24)
	v_mul_f32_e32 v141, 0x42800000, v30
	v_cvt_pk_fp8_f32 v139, v140, v141 op_sel:[0,0,1]
	v_mul_f32_e32 v141, 0x42800000, v3
	v_mul_f32_e32 v142, 0x42800000, v7
	v_mov_b32_e32 v140, v131
	v_cvt_pk_fp8_f32 v140, v141, v142
	v_mul_f32_e32 v142, 0x42800000, v19
	v_mul_f32_e32 v145, 0x42800000, v23
	v_mov_b32_e32 v141, v131
	v_cvt_pk_fp8_f32 v141, v142, v145
	v_mul_f32_e32 v143, 0x42800000, v11
	v_mul_f32_e32 v144, 0x42800000, v15
	v_cvt_pk_fp8_f32 v140, v143, v144 op_sel:[0,0,1]
	v_mul_f32_e32 v142, 0x42800000, v27
	v_mul_f32_e32 v143, 0x42800000, v31
	v_cvt_pk_fp8_f32 v141, v142, v143 op_sel:[0,0,1]
	v_mul_f32_e32 v143, 0x42800000, v4
	v_mul_f32_e32 v144, 0x42800000, v8
	v_mov_b32_e32 v142, v131
	v_cvt_pk_fp8_f32 v142, v143, v144
	v_mul_f32_e32 v144, 0x42800000, v20
	v_mul_f32_e32 v147, 0x42800000, v24
	v_mov_b32_e32 v143, v131
	v_cvt_pk_fp8_f32 v143, v144, v147
	v_mul_f32_e32 v145, 0x42800000, v12
	v_mul_f32_e32 v146, 0x42800000, v16
	v_cvt_pk_fp8_f32 v142, v145, v146 op_sel:[0,0,1]
	v_mul_f32_e32 v144, 0x42800000, v28
	v_mul_f32_e32 v145, 0x42800000, v32
	v_cvt_pk_fp8_f32 v143, v144, v145 op_sel:[0,0,1]
	ds_write_b64 v236, v[136:137] offset:384
	ds_write_b64 v238, v[138:139]
	ds_write_b64 v238, v[140:141] offset:128
	ds_write_b64 v238, v[142:143] offset:256
	v_mul_f32_e32 v137, 0x42800000, v5
	v_mul_f32_e32 v138, 0x42800000, v9
	v_mov_b32_e32 v136, v131
	v_cvt_pk_fp8_f32 v136, v137, v138
	v_mul_f32_e32 v138, 0x42800000, v21
	v_mul_f32_e32 v141, 0x42800000, v25
	v_mov_b32_e32 v137, v131
	v_cvt_pk_fp8_f32 v137, v138, v141
	v_mul_f32_e32 v139, 0x42800000, v13
	v_mul_f32_e32 v140, 0x42800000, v17
	v_cvt_pk_fp8_f32 v136, v139, v140 op_sel:[0,0,1]
	v_mul_f32_e32 v138, 0x42800000, v29
	v_mul_f32_e32 v139, 0x42800000, v33
	v_cvt_pk_fp8_f32 v137, v138, v139 op_sel:[0,0,1]
	ds_write_b64 v238, v[136:137] offset:384
	s_cbranch_vccnz .LBB0_170
	v_lshl_or_b32 v32, s4, 7, v1
	v_or_b32_e32 v2, 39, v32
	v_mul_u32_u24_e32 v4, s26, v2
	v_lshlrev_b32_e32 v2, 2, v4
	v_mov_b32_e32 v3, v131
	s_lshl_b32 s16, s24, 8
	s_mov_b32 s17, s9
	v_lshl_add_u64 v[2:3], s[12:13], 0, v[2:3]
	s_lshl_b64 s[16:17], s[16:17], 2
	v_lshl_add_u64 v[2:3], v[2:3], 0, s[16:17]
	v_lshl_add_u64 v[30:31], v[2:3], 0, v[130:131]
	v_subrev_u32_e32 v2, s26, v4
	v_mov_b32_e32 v3, v131
	v_lshl_add_u64 v[4:5], v[2:3], 2, s[12:13]
	v_lshl_add_u64 v[4:5], v[4:5], 0, s[16:17]
	v_subrev_u32_e32 v2, s26, v2
	v_lshl_add_u64 v[26:27], v[4:5], 0, v[130:131]
	v_lshl_add_u64 v[4:5], v[2:3], 2, s[12:13]
	v_lshl_add_u64 v[4:5], v[4:5], 0, s[16:17]
	v_subrev_u32_e32 v2, s26, v2
	v_lshl_add_u64 v[22:23], v[4:5], 0, v[130:131]
	v_lshl_add_u64 v[4:5], v[2:3], 2, s[12:13]
	v_lshl_add_u64 v[4:5], v[4:5], 0, s[16:17]
	v_subrev_u32_e32 v2, s26, v2
	v_lshl_add_u64 v[18:19], v[4:5], 0, v[130:131]
	v_lshl_add_u64 v[4:5], v[2:3], 2, s[12:13]
	v_lshl_add_u64 v[4:5], v[4:5], 0, s[16:17]
	v_subrev_u32_e32 v2, s26, v2
	v_lshl_add_u64 v[14:15], v[4:5], 0, v[130:131]
	v_lshl_add_u64 v[4:5], v[2:3], 2, s[12:13]
	v_lshl_add_u64 v[4:5], v[4:5], 0, s[16:17]
	v_subrev_u32_e32 v2, s26, v2
	v_lshl_add_u64 v[10:11], v[4:5], 0, v[130:131]
	v_lshl_add_u64 v[4:5], v[2:3], 2, s[12:13]
	v_lshl_add_u64 v[4:5], v[4:5], 0, s[16:17]
	v_subrev_u32_e32 v2, s26, v2
	s_mul_i32 s5, s26, 0xffffffe7
	v_lshl_add_u64 v[6:7], v[4:5], 0, v[130:131]
	v_lshl_add_u64 v[4:5], v[2:3], 2, s[12:13]
	v_add_u32_e32 v2, s5, v2
	v_lshl_add_u64 v[8:9], v[2:3], 2, s[12:13]
	v_subrev_u32_e32 v2, s26, v2
	v_lshl_add_u64 v[12:13], v[2:3], 2, s[12:13]
	v_subrev_u32_e32 v2, s26, v2
	v_lshl_add_u64 v[16:17], v[2:3], 2, s[12:13]
	v_subrev_u32_e32 v2, s26, v2
	v_lshl_add_u64 v[20:21], v[2:3], 2, s[12:13]
	v_subrev_u32_e32 v2, s26, v2
	v_lshl_add_u64 v[24:25], v[2:3], 2, s[12:13]
	v_subrev_u32_e32 v2, s26, v2
	v_mul_u32_u24_e32 v32, s26, v32
	v_lshl_add_u64 v[28:29], v[2:3], 2, s[12:13]
	v_subrev_u32_e32 v2, s26, v2
	v_lshlrev_b32_e32 v32, 2, v32
	v_mov_b32_e32 v33, v131
	v_lshl_add_u64 v[2:3], v[2:3], 2, s[12:13]
	v_lshl_add_u64 v[32:33], s[12:13], 0, v[32:33]
	v_lshl_add_u64 v[4:5], v[4:5], 0, s[16:17]
	v_lshl_add_u64 v[8:9], v[8:9], 0, s[16:17]
	v_lshl_add_u64 v[12:13], v[12:13], 0, s[16:17]
	v_lshl_add_u64 v[16:17], v[16:17], 0, s[16:17]
	v_lshl_add_u64 v[20:21], v[20:21], 0, s[16:17]
	v_lshl_add_u64 v[24:25], v[24:25], 0, s[16:17]
	v_lshl_add_u64 v[28:29], v[28:29], 0, s[16:17]
	v_lshl_add_u64 v[2:3], v[2:3], 0, s[16:17]
	v_lshl_add_u64 v[32:33], v[32:33], 0, s[16:17]
	v_lshl_add_u64 v[4:5], v[4:5], 0, v[130:131]
	v_lshl_add_u64 v[8:9], v[8:9], 0, v[130:131]
	v_lshl_add_u64 v[12:13], v[12:13], 0, v[130:131]
	v_lshl_add_u64 v[16:17], v[16:17], 0, v[130:131]
	v_lshl_add_u64 v[20:21], v[20:21], 0, v[130:131]
	v_lshl_add_u64 v[24:25], v[24:25], 0, v[130:131]
	v_lshl_add_u64 v[28:29], v[28:29], 0, v[130:131]
	v_lshl_add_u64 v[2:3], v[2:3], 0, v[130:131]
	v_lshl_add_u64 v[32:33], v[32:33], 0, v[130:131]
	global_load_dwordx4 v[58:61], v[32:33], off
	global_load_dwordx4 v[62:65], v[2:3], off
	global_load_dwordx4 v[50:53], v[28:29], off
	global_load_dwordx4 v[42:45], v[24:25], off
	global_load_dwordx4 v[54:57], v[20:21], off
	global_load_dwordx4 v[34:37], v[16:17], off
	global_load_dwordx4 v[38:41], v[12:13], off
	global_load_dwordx4 v[46:49], v[8:9], off
	s_nop 0
	global_load_dwordx4 v[2:5], v[4:5], off
	s_nop 0
	global_load_dwordx4 v[6:9], v[6:7], off
	s_nop 0
	global_load_dwordx4 v[10:13], v[10:11], off
	s_nop 0
	global_load_dwordx4 v[14:17], v[14:15], off
	s_nop 0
	global_load_dwordx4 v[18:21], v[18:19], off
	s_nop 0
	global_load_dwordx4 v[22:25], v[22:23], off
	s_nop 0
	global_load_dwordx4 v[26:29], v[26:27], off
	s_nop 0
	global_load_dwordx4 v[30:33], v[30:31], off
	s_branch .LBB0_170
